# weight conversion: nt on every f32 weight tile load incl. the filler conversions in the out and down GEMM phases
# baseline (speedup 1.0000x reference)
.LBB0_99:
	s_andn2_saveexec_b64 s[46:47], s[0:1]
	s_cbranch_execz .LBB0_84
	v_ashrrev_i32_e32 v4, 31, v46
	v_lshrrev_b32_e32 v4, 28, v4
	v_add_u32_e32 v4, v46, v4
	v_ashrrev_i32_e32 v47, 4, v4
	v_lshlrev_b32_e32 v77, 6, v47
	v_or_b32_e32 v6, v77, v162
	s_mov_b32 s0, 0xff93c000
	v_mad_u64_u32 v[4:5], s[0:1], v47, s0, v[2:3]
	v_cmp_gt_i32_e32 vcc, s33, v6
	v_ashrrev_i32_e32 v5, 31, v4
	v_lshl_add_u64 v[4:5], v[4:5], 2, s[22:23]
	v_cndmask_b32_e32 v6, 0, v6, vcc
	v_ashrrev_i32_e32 v7, 31, v6
	v_lshl_add_u64 v[40:41], v[6:7], 2, v[4:5]
	s_mov_b32 s0, 0x1b000
	s_waitcnt lgkmcnt(0)
	v_add_co_u32_e64 v8, s[0:1], s0, v40
	s_nop 1
	v_addc_co_u32_e64 v9, s[0:1], 0, v41, s[0:1]
	s_mov_b32 s0, 0x36000
	s_nop 0
	v_add_co_u32_e64 v12, s[0:1], s0, v40
	global_load_dwordx4 v[4:7], v[40:41], off nt
	s_nop 0
	global_load_dwordx4 v[8:11], v[8:9], off offset:256 nt
	v_addc_co_u32_e64 v13, s[0:1], 0, v41, s[0:1]
	s_mov_b32 s0, 0x51000
	s_nop 0
	v_add_co_u32_e64 v16, s[0:1], s0, v40
	s_nop 1
	v_addc_co_u32_e64 v17, s[0:1], 0, v41, s[0:1]
	s_mov_b32 s0, 0x6c000
	s_nop 0
	v_add_co_u32_e64 v20, s[0:1], s0, v40
	global_load_dwordx4 v[12:15], v[12:13], off offset:512 nt
	s_nop 0
	global_load_dwordx4 v[16:19], v[16:17], off offset:768 nt
	v_addc_co_u32_e64 v21, s[0:1], 0, v41, s[0:1]
	s_mov_b32 s0, 0x87000
	s_nop 0
	v_add_co_u32_e64 v24, s[0:1], s0, v40
	s_nop 1
	v_addc_co_u32_e64 v25, s[0:1], 0, v41, s[0:1]
	s_mov_b32 s0, 0xa2000
	s_nop 0
	v_add_co_u32_e64 v28, s[0:1], s0, v40
	global_load_dwordx4 v[20:23], v[20:21], off offset:1024 nt
	s_nop 0
	global_load_dwordx4 v[24:27], v[24:25], off offset:1280 nt
	v_addc_co_u32_e64 v29, s[0:1], 0, v41, s[0:1]
	s_mov_b32 s0, 0xbd000
	s_nop 0
	v_add_co_u32_e64 v32, s[0:1], s0, v40
	s_nop 1
	v_addc_co_u32_e64 v33, s[0:1], 0, v41, s[0:1]
	s_mov_b32 s0, 0xd8000
	s_nop 0
	v_add_co_u32_e64 v36, s[0:1], s0, v40
	global_load_dwordx4 v[28:31], v[28:29], off offset:1536 nt
	s_nop 0
	global_load_dwordx4 v[32:35], v[32:33], off offset:1792 nt
	v_addc_co_u32_e64 v37, s[0:1], 0, v41, s[0:1]
	s_mov_b32 s0, 0xf3000
	s_nop 0
	v_add_co_u32_e64 v48, s[0:1], s0, v40
	s_nop 1
	v_addc_co_u32_e64 v49, s[0:1], 0, v41, s[0:1]
	s_mov_b32 s0, 0x10e000
	s_nop 0
	v_add_co_u32_e64 v52, s[0:1], s0, v40
	global_load_dwordx4 v[36:39], v[36:37], off offset:2048 nt
	s_nop 0
	global_load_dwordx4 v[48:51], v[48:49], off offset:2304 nt
	v_addc_co_u32_e64 v53, s[0:1], 0, v41, s[0:1]
	s_mov_b32 s0, 0x129000
	s_nop 0
	v_add_co_u32_e64 v56, s[0:1], s0, v40
	s_nop 1
	v_addc_co_u32_e64 v57, s[0:1], 0, v41, s[0:1]
	s_mov_b32 s0, 0x144000
	s_nop 0
	v_add_co_u32_e64 v60, s[0:1], s0, v40
	global_load_dwordx4 v[52:55], v[52:53], off offset:2560 nt
	s_nop 0
	global_load_dwordx4 v[56:59], v[56:57], off offset:2816 nt
	v_addc_co_u32_e64 v61, s[0:1], 0, v41, s[0:1]
	s_mov_b32 s0, 0x15f000
	s_nop 0
	v_add_co_u32_e64 v64, s[0:1], s0, v40
	s_nop 1
	v_addc_co_u32_e64 v65, s[0:1], 0, v41, s[0:1]
	s_mov_b32 s0, 0x17a000
	s_nop 0
	v_add_co_u32_e64 v68, s[0:1], s0, v40
	global_load_dwordx4 v[60:63], v[60:61], off offset:3072 nt
	s_nop 0
	global_load_dwordx4 v[64:67], v[64:65], off offset:3328 nt
	v_addc_co_u32_e64 v69, s[0:1], 0, v41, s[0:1]
	s_mov_b32 s0, 0x195000
	s_nop 0
	v_add_co_u32_e64 v40, s[0:1], s0, v40
	s_nop 1
	v_addc_co_u32_e64 v41, s[0:1], 0, v41, s[0:1]
	global_load_dwordx4 v[68:71], v[68:69], off offset:3584 nt
	s_nop 0
	global_load_dwordx4 v[72:75], v[40:41], off offset:3840 nt
	v_lshlrev_b32_e32 v40, 10, v47
	v_sub_u32_e32 v76, v3, v40
	s_waitcnt vmcnt(0)
	v_cndmask_b32_e32 v4, 0, v4, vcc
	v_cndmask_b32_e32 v5, 0, v5, vcc
	ds_write2_b32 v163, v4, v5 offset1:1
	v_cndmask_b32_e32 v4, 0, v6, vcc
	v_cndmask_b32_e32 v5, 0, v7, vcc
	ds_write2_b32 v163, v4, v5 offset0:2 offset1:3
	v_cndmask_b32_e32 v4, 0, v8, vcc
	v_cndmask_b32_e32 v5, 0, v9, vcc
	v_add_u32_e32 v6, 0x410, v163
	ds_write2_b32 v6, v4, v5 offset1:1
	v_cndmask_b32_e32 v4, 0, v10, vcc
	v_cndmask_b32_e32 v5, 0, v11, vcc
	v_add_u32_e32 v6, 0x418, v163
	ds_write2_b32 v6, v4, v5 offset1:1
	v_cndmask_b32_e32 v4, 0, v12, vcc
	v_cndmask_b32_e32 v5, 0, v13, vcc
	v_add_u32_e32 v6, 0x820, v163
	ds_write2_b32 v6, v4, v5 offset1:1
	v_cndmask_b32_e32 v4, 0, v14, vcc
	v_cndmask_b32_e32 v5, 0, v15, vcc
	v_add_u32_e32 v6, 0x828, v163
	ds_write2_b32 v6, v4, v5 offset1:1
	v_cndmask_b32_e32 v4, 0, v16, vcc
	v_cndmask_b32_e32 v5, 0, v17, vcc
	v_add_u32_e32 v6, 0xc30, v163
	ds_write2_b32 v6, v4, v5 offset1:1
	v_cndmask_b32_e32 v4, 0, v18, vcc
	v_cndmask_b32_e32 v5, 0, v19, vcc
	v_add_u32_e32 v6, 0xc38, v163
	ds_write2_b32 v6, v4, v5 offset1:1
	v_cndmask_b32_e32 v4, 0, v20, vcc
	v_cndmask_b32_e32 v5, 0, v21, vcc
	v_add_u32_e32 v6, 0x1040, v163
	ds_write2_b32 v6, v4, v5 offset1:1
	v_cndmask_b32_e32 v4, 0, v22, vcc
	v_cndmask_b32_e32 v5, 0, v23, vcc
	v_add_u32_e32 v6, 0x1048, v163
	ds_write2_b32 v6, v4, v5 offset1:1
	v_cndmask_b32_e32 v4, 0, v24, vcc
	v_cndmask_b32_e32 v5, 0, v25, vcc
	v_add_u32_e32 v6, 0x1450, v163
	ds_write2_b32 v6, v4, v5 offset1:1
	v_cndmask_b32_e32 v4, 0, v26, vcc
	v_cndmask_b32_e32 v5, 0, v27, vcc
	v_add_u32_e32 v6, 0x1458, v163
	ds_write2_b32 v6, v4, v5 offset1:1
	v_cndmask_b32_e32 v4, 0, v28, vcc
	v_cndmask_b32_e32 v5, 0, v29, vcc
	v_add_u32_e32 v6, 0x1860, v163
	ds_write2_b32 v6, v4, v5 offset1:1
	v_cndmask_b32_e32 v4, 0, v30, vcc
	v_cndmask_b32_e32 v5, 0, v31, vcc
	v_add_u32_e32 v6, 0x1868, v163
	ds_write2_b32 v6, v4, v5 offset1:1
	v_cndmask_b32_e32 v4, 0, v32, vcc
	v_cndmask_b32_e32 v5, 0, v33, vcc
	v_add_u32_e32 v6, 0x1c70, v163
	ds_write2_b32 v6, v4, v5 offset1:1
	v_cndmask_b32_e32 v4, 0, v34, vcc
	v_cndmask_b32_e32 v5, 0, v35, vcc
	v_add_u32_e32 v6, 0x1c78, v163
	ds_write2_b32 v6, v4, v5 offset1:1
	v_cndmask_b32_e32 v4, 0, v36, vcc
	v_cndmask_b32_e32 v5, 0, v37, vcc
	v_add_u32_e32 v6, 0x2080, v163
	ds_write2_b32 v6, v4, v5 offset1:1
	v_cndmask_b32_e32 v4, 0, v38, vcc
	v_cndmask_b32_e32 v5, 0, v39, vcc
	v_add_u32_e32 v6, 0x2088, v163
	ds_write2_b32 v6, v4, v5 offset1:1
	v_cndmask_b32_e32 v4, 0, v48, vcc
	v_cndmask_b32_e32 v5, 0, v49, vcc
	v_add_u32_e32 v6, 0x2490, v163
	ds_write2_b32 v6, v4, v5 offset1:1
	v_cndmask_b32_e32 v4, 0, v50, vcc
	v_cndmask_b32_e32 v5, 0, v51, vcc
	v_add_u32_e32 v6, 0x2498, v163
	ds_write2_b32 v6, v4, v5 offset1:1
	v_cndmask_b32_e32 v4, 0, v52, vcc
	v_cndmask_b32_e32 v5, 0, v53, vcc
	v_add_u32_e32 v6, 0x28a0, v163
	ds_write2_b32 v6, v4, v5 offset1:1
	v_cndmask_b32_e32 v4, 0, v54, vcc
	v_cndmask_b32_e32 v5, 0, v55, vcc
	v_add_u32_e32 v6, 0x28a8, v163
	ds_write2_b32 v6, v4, v5 offset1:1
	v_cndmask_b32_e32 v4, 0, v56, vcc
	v_cndmask_b32_e32 v5, 0, v57, vcc
	v_add_u32_e32 v6, 0x2cb0, v163
	ds_write2_b32 v6, v4, v5 offset1:1
	v_cndmask_b32_e32 v4, 0, v58, vcc
	v_cndmask_b32_e32 v5, 0, v59, vcc
	v_add_u32_e32 v6, 0x2cb8, v163
	ds_write2_b32 v6, v4, v5 offset1:1
	v_cndmask_b32_e32 v4, 0, v60, vcc
	v_cndmask_b32_e32 v5, 0, v61, vcc
	v_add_u32_e32 v6, 0x30c0, v163
	ds_write2_b32 v6, v4, v5 offset1:1
	v_cndmask_b32_e32 v4, 0, v62, vcc
	v_cndmask_b32_e32 v5, 0, v63, vcc
	v_add_u32_e32 v6, 0x30c8, v163
	ds_write2_b32 v6, v4, v5 offset1:1
	v_cndmask_b32_e32 v4, 0, v64, vcc
	v_cndmask_b32_e32 v5, 0, v65, vcc
	v_add_u32_e32 v6, 0x34d0, v163
	ds_write2_b32 v6, v4, v5 offset1:1
	v_cndmask_b32_e32 v4, 0, v66, vcc
	v_cndmask_b32_e32 v5, 0, v67, vcc
	v_add_u32_e32 v6, 0x34d8, v163
	ds_write2_b32 v6, v4, v5 offset1:1
	v_cndmask_b32_e32 v4, 0, v68, vcc
	v_cndmask_b32_e32 v5, 0, v69, vcc
	v_add_u32_e32 v6, 0x38e0, v163
	ds_write2_b32 v6, v4, v5 offset1:1
	v_cndmask_b32_e32 v4, 0, v70, vcc
	v_cndmask_b32_e32 v5, 0, v71, vcc
	v_add_u32_e32 v6, 0x38e8, v163
	ds_write2_b32 v6, v4, v5 offset1:1
	v_cndmask_b32_e32 v4, 0, v72, vcc
	v_cndmask_b32_e32 v5, 0, v73, vcc
	v_add_u32_e32 v6, 0x3cf0, v163
	ds_write2_b32 v6, v4, v5 offset1:1
	v_cndmask_b32_e32 v4, 0, v74, vcc
	v_cndmask_b32_e32 v5, 0, v75, vcc
	v_add_u32_e32 v6, 0x3cf8, v163
	ds_write2_b32 v6, v4, v5 offset1:1
	v_add_u32_e32 v40, 0x400, v165
	ds_read2_b32 v[24:25], v165 offset1:8
	ds_read2_b32 v[26:27], v165 offset0:65 offset1:73
	ds_read2_b32 v[28:29], v165 offset0:130 offset1:138
	ds_read2_b32 v[30:31], v165 offset0:195 offset1:203
	ds_read2_b32 v[32:33], v40 offset0:4 offset1:12
	ds_read2_b32 v[34:35], v40 offset0:69 offset1:77
	ds_read2_b32 v[36:37], v40 offset0:134 offset1:142
	ds_read2_b32 v[38:39], v40 offset0:199 offset1:207
	ds_read2_b32 v[8:9], v165 offset0:16 offset1:24
	ds_read2_b32 v[10:11], v165 offset0:81 offset1:89
	ds_read2_b32 v[12:13], v165 offset0:146 offset1:154
	ds_read2_b32 v[14:15], v165 offset0:211 offset1:219
	ds_read2_b32 v[16:17], v40 offset0:20 offset1:28
	ds_read2_b32 v[18:19], v40 offset0:85 offset1:93
	ds_read2_b32 v[20:21], v40 offset0:150 offset1:158
	ds_read2_b32 v[22:23], v40 offset0:215 offset1:223
	v_or_b32_e32 v6, v77, v164
	v_ashrrev_i32_e32 v77, 31, v76
	v_lshl_add_u64 v[4:5], v[76:77], 1, v[120:121]
	v_cmp_gt_i32_e32 vcc, s33, v6
	s_and_saveexec_b64 s[0:1], vcc
	s_cbranch_execz .LBB0_102
	v_ashrrev_i32_e32 v7, 31, v6
	v_lshlrev_b64 v[52:53], 11, v[6:7]
	s_waitcnt lgkmcnt(14)
	v_cvt_pk_bf16_f32 v48, v24, v26
	s_waitcnt lgkmcnt(12)
	v_cvt_pk_bf16_f32 v49, v28, v30
	s_waitcnt lgkmcnt(10)
	v_cvt_pk_bf16_f32 v50, v32, v34
	s_waitcnt lgkmcnt(8)
	v_cvt_pk_bf16_f32 v51, v36, v38
	v_lshl_add_u64 v[52:53], v[4:5], 0, v[52:53]
	global_store_dwordx4 v[52:53], v[48:51], off

.LBB0_1019:
	s_movk_i32 s0, 0x6cf
	v_cmp_lt_i32_e32 vcc, s0, v3
	s_and_saveexec_b64 s[0:1], vcc
	s_xor_b64 s[0:1], exec, s[0:1]
	s_cbranch_execz .LBB0_1029
	s_movk_i32 s18, 0x84f
	v_cmp_lt_u32_e32 vcc, s18, v3
	s_and_saveexec_b64 s[18:19], vcc
	s_xor_b64 s[18:19], exec, s[18:19]
	s_cbranch_execz .LBB0_1026
	s_movk_i32 s20, 0x94f
	v_and_b32_e32 v10, 0x3c0, v52
	v_cmp_lt_u32_e32 vcc, s20, v3
	v_or_b32_e32 v11, v10, v9
	v_lshlrev_b32_e32 v10, 1, v10
	s_and_saveexec_b64 s[20:21], vcc
	s_xor_b64 s[20:21], exec, s[20:21]
	s_cbranch_execz .LBB0_1023
	v_add_u32_e32 v86, 0xfffff6b0, v3
	v_mov_b32_e32 v12, s67
	v_mov_b32_e32 v13, s65
	v_cmp_gt_u32_e32 vcc, s76, v86
	s_waitcnt lgkmcnt(0)
	v_mov_b32_e32 v14, s64
	v_and_b32_e32 v130, 0x7800000, v54
	v_cndmask_b32_e32 v13, v12, v13, vcc
	v_mov_b32_e32 v12, s66
	v_cndmask_b32_e32 v12, v12, v14, vcc
	v_lshl_add_u64 v[12:13], v[12:13], 0, s[4:5]
	v_add_u32_e32 v87, 0xffffdac0, v53
	s_movk_i32 s22, 0x7c0
	v_lshl_add_u64 v[12:13], v[12:13], 0, v[130:131]
	v_lshl_add_u64 v[84:85], s[8:9], 0, v[130:131]
	v_and_or_b32 v14, v87, s22, v48
	v_lshlrev_b32_e32 v130, 13, v11
	v_lshl_add_u64 v[12:13], v[12:13], 0, v[130:131]
	v_lshlrev_b32_e32 v130, 2, v14
	v_lshl_add_u64 v[76:77], v[12:13], 0, v[130:131]
	s_mov_b32 s23, 0x8000
	v_add_co_u32_e32 v16, vcc, s23, v76
	s_mov_b32 s25, 0x10000
	s_nop 0
	v_addc_co_u32_e32 v17, vcc, 0, v77, vcc
	v_add_co_u32_e32 v20, vcc, s25, v76
	s_mov_b32 s24, 0x18000
	s_nop 0
	v_addc_co_u32_e32 v21, vcc, 0, v77, vcc
	v_add_co_u32_e32 v24, vcc, s24, v76
	s_mov_b32 s22, 0x20000
	s_nop 0
	v_addc_co_u32_e32 v25, vcc, 0, v77, vcc
	v_add_co_u32_e32 v28, vcc, s22, v76
	s_mov_b32 s22, 0x28000
	s_nop 0
	v_addc_co_u32_e32 v29, vcc, 0, v77, vcc
	v_add_co_u32_e32 v32, vcc, s22, v76
	s_mov_b32 s22, 0x30000
	s_nop 0
	v_addc_co_u32_e32 v33, vcc, 0, v77, vcc
	v_add_co_u32_e32 v36, vcc, s22, v76
	s_mov_b32 s22, 0x38000
	s_nop 0
	v_addc_co_u32_e32 v37, vcc, 0, v77, vcc
	v_add_co_u32_e32 v40, vcc, s22, v76
	s_mov_b32 s22, 0x40000
	s_nop 0
	v_addc_co_u32_e32 v41, vcc, 0, v77, vcc
	v_add_co_u32_e32 v44, vcc, s22, v76
	s_mov_b32 s22, 0x48000
	s_nop 0
	v_addc_co_u32_e32 v45, vcc, 0, v77, vcc
	v_add_co_u32_e32 v56, vcc, s22, v76
	s_mov_b32 s22, 0x50000
	s_nop 0
	v_addc_co_u32_e32 v57, vcc, 0, v77, vcc
	v_add_co_u32_e32 v60, vcc, s22, v76
	s_mov_b32 s22, 0x58000
	s_nop 0
	v_addc_co_u32_e32 v61, vcc, 0, v77, vcc
	v_add_co_u32_e32 v64, vcc, s22, v76
	s_mov_b32 s22, 0x60000
	s_nop 0
	v_addc_co_u32_e32 v65, vcc, 0, v77, vcc
	v_add_co_u32_e32 v68, vcc, s22, v76
	s_mov_b32 s22, 0x68000
	s_nop 0
	v_addc_co_u32_e32 v69, vcc, 0, v77, vcc
	v_add_co_u32_e32 v72, vcc, s22, v76
	s_mov_b32 s22, 0x70000
	s_nop 0
	v_addc_co_u32_e32 v73, vcc, 0, v77, vcc
	v_add_co_u32_e32 v78, vcc, s22, v76
	s_mov_b32 s22, 0x78000
	s_nop 0
	v_addc_co_u32_e32 v79, vcc, 0, v77, vcc
	v_add_co_u32_e32 v80, vcc, s22, v76
	global_load_dwordx4 v[12:15], v[76:77], off nt
	s_nop 0
	global_load_dwordx4 v[16:19], v[16:17], off nt
	v_addc_co_u32_e32 v81, vcc, 0, v77, vcc
	global_load_dwordx4 v[20:23], v[20:21], off nt
	s_nop 0
	global_load_dwordx4 v[24:27], v[24:25], off nt
	s_nop 0
	global_load_dwordx4 v[28:31], v[28:29], off nt
	s_nop 0
	global_load_dwordx4 v[32:35], v[32:33], off nt
	s_nop 0
	global_load_dwordx4 v[36:39], v[36:37], off nt
	s_nop 0
	global_load_dwordx4 v[40:43], v[40:41], off nt
	s_nop 0
	global_load_dwordx4 v[44:47], v[44:45], off nt
	s_nop 0
	global_load_dwordx4 v[56:59], v[56:57], off nt
	s_nop 0
	global_load_dwordx4 v[60:63], v[60:61], off nt
	s_nop 0
	global_load_dwordx4 v[64:67], v[64:65], off nt
	s_nop 0
	global_load_dwordx4 v[68:71], v[68:69], off nt
	s_nop 0
	global_load_dwordx4 v[72:75], v[72:73], off nt
	s_nop 0
	global_load_dwordx4 v[76:79], v[78:79], off nt
	s_nop 0
	global_load_dwordx4 v[80:83], v[80:81], off nt
	v_add_u32_e32 v11, 0x410, v49
	s_waitcnt vmcnt(0)
	ds_write2_b32 v49, v12, v13 offset1:1
	ds_write2_b32 v49, v14, v15 offset0:2 offset1:3
	ds_write2_b32 v11, v16, v17 offset1:1
	v_add_u32_e32 v11, 0x418, v49
	ds_write2_b32 v11, v18, v19 offset1:1
	v_add_u32_e32 v11, 0x820, v49
	ds_write2_b32 v11, v20, v21 offset1:1
	v_add_u32_e32 v11, 0x828, v49
	ds_write2_b32 v11, v22, v23 offset1:1
	v_add_u32_e32 v11, 0xc30, v49
	ds_write2_b32 v11, v24, v25 offset1:1
	v_add_u32_e32 v11, 0xc38, v49
	ds_write2_b32 v11, v26, v27 offset1:1
	v_add_u32_e32 v11, 0x1040, v49
	ds_write2_b32 v11, v28, v29 offset1:1
	v_add_u32_e32 v11, 0x1048, v49
	ds_write2_b32 v11, v30, v31 offset1:1
	v_add_u32_e32 v11, 0x1450, v49
	ds_write2_b32 v11, v32, v33 offset1:1
	v_add_u32_e32 v11, 0x1458, v49
	ds_write2_b32 v11, v34, v35 offset1:1
	v_add_u32_e32 v11, 0x1860, v49
	ds_write2_b32 v11, v36, v37 offset1:1
	v_add_u32_e32 v11, 0x1868, v49
	ds_write2_b32 v11, v38, v39 offset1:1
	v_add_u32_e32 v11, 0x1c70, v49
	ds_write2_b32 v11, v40, v41 offset1:1
	v_add_u32_e32 v11, 0x1c78, v49
	ds_write2_b32 v11, v42, v43 offset1:1
	v_add_u32_e32 v11, 0x2080, v49
	ds_write2_b32 v11, v44, v45 offset1:1
	v_add_u32_e32 v11, 0x2088, v49
	ds_write2_b32 v11, v46, v47 offset1:1
	v_add_u32_e32 v11, 0x2490, v49
	ds_write2_b32 v11, v56, v57 offset1:1
	v_add_u32_e32 v11, 0x2498, v49
	ds_write2_b32 v11, v58, v59 offset1:1
	v_add_u32_e32 v11, 0x28a0, v49
	ds_write2_b32 v11, v60, v61 offset1:1
	v_add_u32_e32 v11, 0x28a8, v49
	ds_write2_b32 v11, v62, v63 offset1:1
	v_add_u32_e32 v11, 0x2cb0, v49
	ds_write2_b32 v11, v64, v65 offset1:1
	v_add_u32_e32 v11, 0x2cb8, v49
	ds_write2_b32 v11, v66, v67 offset1:1
	v_add_u32_e32 v11, 0x30c0, v49
	ds_write2_b32 v11, v68, v69 offset1:1
	v_add_u32_e32 v11, 0x30c8, v49
	ds_write2_b32 v11, v70, v71 offset1:1
	v_add_u32_e32 v11, 0x34d0, v49
	ds_write2_b32 v11, v72, v73 offset1:1
	v_add_u32_e32 v11, 0x34d8, v49
	ds_write2_b32 v11, v74, v75 offset1:1
	v_add_u32_e32 v11, 0x38e0, v49
	ds_write2_b32 v11, v76, v77 offset1:1
	v_add_u32_e32 v11, 0x38e8, v49
	ds_write2_b32 v11, v78, v79 offset1:1
	v_add_u32_e32 v11, 0x3cf0, v49
	ds_write2_b32 v11, v80, v81 offset1:1
	v_add_u32_e32 v11, 0x3cf8, v49
	ds_write2_b32 v11, v82, v83 offset1:1
	v_add_u32_e32 v56, 0x400, v51
	ds_read2_b32 v[14:15], v51 offset0:65 offset1:73
	ds_read2_b32 v[16:17], v51 offset0:130 offset1:138
	ds_read2_b32 v[18:19], v51 offset0:195 offset1:203
	ds_read2_b32 v[20:21], v56 offset0:4 offset1:12
	ds_read2_b32 v[22:23], v56 offset0:69 offset1:77
	ds_read2_b32 v[24:25], v56 offset0:134 offset1:142
	ds_read2_b32 v[26:27], v56 offset0:199 offset1:207
	ds_read2_b32 v[28:29], v51 offset1:8
	ds_read2_b32 v[30:31], v51 offset0:16 offset1:24
	ds_read2_b32 v[32:33], v51 offset0:81 offset1:89
	ds_read2_b32 v[34:35], v51 offset0:146 offset1:154
	ds_read2_b32 v[36:37], v51 offset0:211 offset1:219
	ds_read2_b32 v[38:39], v56 offset0:20 offset1:28
	ds_read2_b32 v[40:41], v56 offset0:85 offset1:93
	ds_read2_b32 v[42:43], v56 offset0:150 offset1:158
	ds_read2_b32 v[44:45], v56 offset0:215 offset1:223
	s_movk_i32 s22, 0x1fff
	v_mov_b32_e32 v11, v131
	v_cmp_lt_u32_e32 vcc, s22, v86
	v_lshl_add_u64 v[10:11], v[84:85], 0, v[10:11]
	v_lshlrev_b32_e32 v130, 1, v2
	v_cndmask_b32_e32 v12, 0, v229, vcc
	v_lshl_add_u64 v[46:47], v[10:11], 0, v[130:131]
	v_lshlrev_b32_e32 v10, 1, v87
	v_and_b32_e32 v10, 0xf00, v10
	v_and_or_b32 v11, v87, 64, v12
	v_or3_b32 v57, v11, v10, v50
	v_lshlrev_b32_e32 v130, 11, v57
	v_lshl_add_u64 v[46:47], v[46:47], 0, v[130:131]
	s_waitcnt lgkmcnt(8)
	v_cvt_pk_bf16_f32 v10, v28, v14
	v_cvt_pk_bf16_f32 v11, v16, v18
	v_cvt_pk_bf16_f32 v12, v20, v22
	v_cvt_pk_bf16_f32 v13, v24, v26
	v_add_co_u32_e32 v14, vcc, s88, v46
	global_store_dwordx4 v[46:47], v[10:13], off
	s_mov_b32 s77, 0x8000
	s_nop 0
	v_cvt_pk_bf16_f32 v10, v29, v15
	v_cvt_pk_bf16_f32 v11, v17, v19
	v_cvt_pk_bf16_f32 v12, v21, v23
	v_cvt_pk_bf16_f32 v13, v25, v27
	v_addc_co_u32_e32 v15, vcc, 0, v47, vcc
	global_store_dwordx4 v[14:15], v[10:13], off
	v_add_co_u32_e32 v14, vcc, s23, v46
	s_waitcnt lgkmcnt(6)
	v_cvt_pk_bf16_f32 v10, v30, v32
	s_waitcnt lgkmcnt(4)
	v_cvt_pk_bf16_f32 v11, v34, v36
	s_waitcnt lgkmcnt(2)
	v_cvt_pk_bf16_f32 v12, v38, v40
	s_waitcnt lgkmcnt(0)
	v_cvt_pk_bf16_f32 v13, v42, v44
	v_addc_co_u32_e32 v15, vcc, 0, v47, vcc
	global_store_dwordx4 v[14:15], v[10:13], off
	v_add_co_u32_e32 v14, vcc, s82, v46
	s_nop 0
	v_cvt_pk_bf16_f32 v10, v31, v33
	v_cvt_pk_bf16_f32 v11, v35, v37
	v_cvt_pk_bf16_f32 v12, v39, v41
	v_cvt_pk_bf16_f32 v13, v43, v45
	v_addc_co_u32_e32 v15, vcc, 0, v47, vcc
	global_store_dwordx4 v[14:15], v[10:13], off
	ds_read2_b32 v[14:15], v51 offset0:97 offset1:105
	ds_read2_b32 v[16:17], v51 offset0:162 offset1:170
	ds_read2_b32 v[18:19], v51 offset0:227 offset1:235
	ds_read2_b32 v[20:21], v56 offset0:36 offset1:44
	ds_read2_b32 v[22:23], v56 offset0:101 offset1:109
	ds_read2_b32 v[24:25], v56 offset0:166 offset1:174
	ds_read2_b32 v[26:27], v56 offset0:231 offset1:239
	ds_read2_b32 v[28:29], v51 offset0:32 offset1:40
	ds_read2_b32 v[30:31], v51 offset0:48 offset1:56
	ds_read2_b32 v[32:33], v51 offset0:113 offset1:121
	ds_read2_b32 v[34:35], v51 offset0:178 offset1:186
	ds_read2_b32 v[36:37], v51 offset0:243 offset1:251
	ds_read2_b32 v[38:39], v56 offset0:52 offset1:60
	ds_read2_b32 v[40:41], v56 offset0:117 offset1:125
	ds_read2_b32 v[42:43], v56 offset0:182 offset1:190
	ds_read2_b32 v[44:45], v56 offset0:247 offset1:255
	v_add_co_u32_e32 v56, vcc, s25, v46
	s_mov_b32 s22, 0x14000
	s_nop 0
	v_addc_co_u32_e32 v57, vcc, 0, v47, vcc
	s_waitcnt lgkmcnt(8)
	v_cvt_pk_bf16_f32 v10, v28, v14
	v_cvt_pk_bf16_f32 v11, v16, v18
	v_cvt_pk_bf16_f32 v12, v20, v22
	v_cvt_pk_bf16_f32 v13, v24, v26
	v_add_co_u32_e32 v14, vcc, s22, v46
	global_store_dwordx4 v[56:57], v[10:13], off
	s_mov_b32 s80, 0x10000
	s_mov_b32 s83, 0x18000
	v_cvt_pk_bf16_f32 v10, v29, v15
	v_cvt_pk_bf16_f32 v11, v17, v19
	v_cvt_pk_bf16_f32 v12, v21, v23
	v_cvt_pk_bf16_f32 v13, v25, v27
	v_addc_co_u32_e32 v15, vcc, 0, v47, vcc
	global_store_dwordx4 v[14:15], v[10:13], off
	v_add_co_u32_e32 v14, vcc, s24, v46
	s_waitcnt lgkmcnt(6)
	v_cvt_pk_bf16_f32 v10, v30, v32
	s_waitcnt lgkmcnt(4)
	v_cvt_pk_bf16_f32 v11, v34, v36
	s_waitcnt lgkmcnt(2)
	v_cvt_pk_bf16_f32 v12, v38, v40
	s_waitcnt lgkmcnt(0)
	v_cvt_pk_bf16_f32 v13, v42, v44
	v_addc_co_u32_e32 v15, vcc, 0, v47, vcc
	global_store_dwordx4 v[14:15], v[10:13], off
	v_add_co_u32_e32 v14, vcc, 0x1c000, v46
	s_nop 0
	v_cvt_pk_bf16_f32 v10, v31, v33
	v_cvt_pk_bf16_f32 v11, v35, v37
	v_cvt_pk_bf16_f32 v12, v39, v41
	v_cvt_pk_bf16_f32 v13, v43, v45
	v_addc_co_u32_e32 v15, vcc, 0, v47, vcc
	global_store_dwordx4 v[14:15], v[10:13], off
.LBB0_1023:
	s_andn2_saveexec_b64 s[20:21], s[20:21]
	s_cbranch_execz .LBB0_1025
	v_and_b32_e32 v12, 0x3fc0, v53
	v_add_u32_e32 v84, 0xffffdec0, v12
	v_lshlrev_b32_e32 v130, 12, v11
	v_or_b32_e32 v12, v84, v48
	s_waitcnt lgkmcnt(0)
	v_lshl_add_u64 v[14:15], s[10:11], 0, v[130:131]
	v_mov_b32_e32 v13, v131
	v_lshl_add_u64 v[76:77], v[12:13], 2, v[14:15]
	v_add_co_u32_e32 v16, vcc, 0x4000, v76
	s_mov_b32 s22, 0x20000
	s_nop 0
	v_addc_co_u32_e32 v17, vcc, 0, v77, vcc
	v_add_co_u32_e32 v20, vcc, 0x8000, v76
	global_load_dwordx4 v[12:15], v[76:77], off nt
	s_nop 0
	global_load_dwordx4 v[16:19], v[16:17], off nt
	v_addc_co_u32_e32 v21, vcc, 0, v77, vcc
	v_add_co_u32_e32 v24, vcc, 0xc000, v76
	s_nop 1
	v_addc_co_u32_e32 v25, vcc, 0, v77, vcc
	v_add_co_u32_e32 v28, vcc, 0x10000, v76
	global_load_dwordx4 v[20:23], v[20:21], off nt
	s_nop 0
	global_load_dwordx4 v[24:27], v[24:25], off nt
	v_addc_co_u32_e32 v29, vcc, 0, v77, vcc
	v_add_co_u32_e32 v32, vcc, 0x14000, v76
	s_nop 1
	v_addc_co_u32_e32 v33, vcc, 0, v77, vcc
	v_add_co_u32_e32 v36, vcc, 0x18000, v76
	global_load_dwordx4 v[28:31], v[28:29], off nt
	s_nop 0
	global_load_dwordx4 v[32:35], v[32:33], off nt
	v_addc_co_u32_e32 v37, vcc, 0, v77, vcc
	v_add_co_u32_e32 v40, vcc, 0x1c000, v76
	s_nop 1
	v_addc_co_u32_e32 v41, vcc, 0, v77, vcc
	v_add_co_u32_e32 v44, vcc, s22, v76
	global_load_dwordx4 v[36:39], v[36:37], off nt
	s_nop 0
	global_load_dwordx4 v[40:43], v[40:41], off nt
	v_addc_co_u32_e32 v45, vcc, 0, v77, vcc
	v_add_co_u32_e32 v56, vcc, 0x24000, v76
	s_nop 1
	v_addc_co_u32_e32 v57, vcc, 0, v77, vcc
	v_add_co_u32_e32 v60, vcc, 0x28000, v76
	global_load_dwordx4 v[44:47], v[44:45], off nt
	s_nop 0
	global_load_dwordx4 v[56:59], v[56:57], off nt
	v_addc_co_u32_e32 v61, vcc, 0, v77, vcc
	v_add_co_u32_e32 v64, vcc, 0x2c000, v76
	s_nop 1
	v_addc_co_u32_e32 v65, vcc, 0, v77, vcc
	v_add_co_u32_e32 v68, vcc, 0x30000, v76
	global_load_dwordx4 v[60:63], v[60:61], off nt
	s_nop 0
	global_load_dwordx4 v[64:67], v[64:65], off nt
	v_addc_co_u32_e32 v69, vcc, 0, v77, vcc
	v_add_co_u32_e32 v72, vcc, 0x34000, v76
	s_nop 1
	v_addc_co_u32_e32 v73, vcc, 0, v77, vcc
	v_add_co_u32_e32 v78, vcc, 0x38000, v76
	global_load_dwordx4 v[68:71], v[68:69], off nt
	s_nop 0
	global_load_dwordx4 v[72:75], v[72:73], off nt
	v_addc_co_u32_e32 v79, vcc, 0, v77, vcc
	v_add_co_u32_e32 v80, vcc, 0x3c000, v76
	s_nop 1
	v_addc_co_u32_e32 v81, vcc, 0, v77, vcc
	global_load_dwordx4 v[76:79], v[78:79], off nt
	s_nop 0
	global_load_dwordx4 v[80:83], v[80:81], off nt
	v_add_u32_e32 v11, 0x410, v49
	s_waitcnt vmcnt(0)
	ds_write2_b32 v49, v12, v13 offset1:1
	ds_write2_b32 v49, v14, v15 offset0:2 offset1:3
	ds_write2_b32 v11, v16, v17 offset1:1
	v_add_u32_e32 v11, 0x418, v49
	ds_write2_b32 v11, v18, v19 offset1:1
	v_add_u32_e32 v11, 0x820, v49
	ds_write2_b32 v11, v20, v21 offset1:1
	v_add_u32_e32 v11, 0x828, v49
	ds_write2_b32 v11, v22, v23 offset1:1
	v_add_u32_e32 v11, 0xc30, v49
	ds_write2_b32 v11, v24, v25 offset1:1
	v_add_u32_e32 v11, 0xc38, v49
	ds_write2_b32 v11, v26, v27 offset1:1
	v_add_u32_e32 v11, 0x1040, v49
	ds_write2_b32 v11, v28, v29 offset1:1
	v_add_u32_e32 v11, 0x1048, v49
	ds_write2_b32 v11, v30, v31 offset1:1
	v_add_u32_e32 v11, 0x1450, v49
	ds_write2_b32 v11, v32, v33 offset1:1
	v_add_u32_e32 v11, 0x1458, v49
	ds_write2_b32 v11, v34, v35 offset1:1
	v_add_u32_e32 v11, 0x1860, v49
	ds_write2_b32 v11, v36, v37 offset1:1
	v_add_u32_e32 v11, 0x1868, v49
	ds_write2_b32 v11, v38, v39 offset1:1
	v_add_u32_e32 v11, 0x1c70, v49
	ds_write2_b32 v11, v40, v41 offset1:1
	v_add_u32_e32 v11, 0x1c78, v49
	ds_write2_b32 v11, v42, v43 offset1:1
	v_add_u32_e32 v11, 0x2080, v49
	ds_write2_b32 v11, v44, v45 offset1:1
	v_add_u32_e32 v11, 0x2088, v49
	ds_write2_b32 v11, v46, v47 offset1:1
	v_add_u32_e32 v11, 0x2490, v49
	ds_write2_b32 v11, v56, v57 offset1:1
	v_add_u32_e32 v11, 0x2498, v49
	ds_write2_b32 v11, v58, v59 offset1:1
	v_add_u32_e32 v11, 0x28a0, v49
	ds_write2_b32 v11, v60, v61 offset1:1
	v_add_u32_e32 v11, 0x28a8, v49
	ds_write2_b32 v11, v62, v63 offset1:1
	v_add_u32_e32 v11, 0x2cb0, v49
	ds_write2_b32 v11, v64, v65 offset1:1
	v_add_u32_e32 v11, 0x2cb8, v49
	ds_write2_b32 v11, v66, v67 offset1:1
	v_add_u32_e32 v11, 0x30c0, v49
	ds_write2_b32 v11, v68, v69 offset1:1
	v_add_u32_e32 v11, 0x30c8, v49
	ds_write2_b32 v11, v70, v71 offset1:1
	v_add_u32_e32 v11, 0x34d0, v49
	ds_write2_b32 v11, v72, v73 offset1:1
	v_add_u32_e32 v11, 0x34d8, v49
	ds_write2_b32 v11, v74, v75 offset1:1
	v_add_u32_e32 v11, 0x38e0, v49
	ds_write2_b32 v11, v76, v77 offset1:1
	v_add_u32_e32 v11, 0x38e8, v49
	ds_write2_b32 v11, v78, v79 offset1:1
	v_add_u32_e32 v11, 0x3cf0, v49
	ds_write2_b32 v11, v80, v81 offset1:1
	v_add_u32_e32 v11, 0x3cf8, v49
	ds_write2_b32 v11, v82, v83 offset1:1
	v_add_u32_e32 v56, 0x400, v51
	ds_read2_b32 v[14:15], v51 offset0:65 offset1:73
	ds_read2_b32 v[16:17], v51 offset0:130 offset1:138
	ds_read2_b32 v[18:19], v51 offset0:195 offset1:203
	ds_read2_b32 v[20:21], v56 offset0:4 offset1:12
	ds_read2_b32 v[22:23], v56 offset0:69 offset1:77
	ds_read2_b32 v[24:25], v56 offset0:134 offset1:142
	ds_read2_b32 v[26:27], v56 offset0:199 offset1:207
	ds_read2_b32 v[28:29], v51 offset1:8
	ds_read2_b32 v[30:31], v51 offset0:16 offset1:24
	ds_read2_b32 v[32:33], v51 offset0:81 offset1:89
	ds_read2_b32 v[34:35], v51 offset0:146 offset1:154
	ds_read2_b32 v[36:37], v51 offset0:211 offset1:219
	ds_read2_b32 v[38:39], v56 offset0:20 offset1:28
	ds_read2_b32 v[40:41], v56 offset0:85 offset1:93
	ds_read2_b32 v[42:43], v56 offset0:150 offset1:158
	ds_read2_b32 v[44:45], v56 offset0:215 offset1:223
	v_mov_b32_e32 v11, v131
	v_or_b32_e32 v57, v84, v50
	v_lshl_add_u64 v[46:47], v[4:5], 0, v[10:11]
	v_lshlrev_b32_e32 v130, 11, v57
	v_lshl_add_u64 v[46:47], v[46:47], 0, v[130:131]
	s_waitcnt lgkmcnt(8)
	v_cvt_pk_bf16_f32 v10, v28, v14
	v_cvt_pk_bf16_f32 v11, v16, v18
	v_cvt_pk_bf16_f32 v12, v20, v22
	v_cvt_pk_bf16_f32 v13, v24, v26
	v_add_co_u32_e32 v14, vcc, s88, v46
	global_store_dwordx4 v[46:47], v[10:13], off
	s_nop 1
	v_cvt_pk_bf16_f32 v10, v29, v15
	v_cvt_pk_bf16_f32 v11, v17, v19
	v_cvt_pk_bf16_f32 v12, v21, v23
	v_cvt_pk_bf16_f32 v13, v25, v27
	v_addc_co_u32_e32 v15, vcc, 0, v47, vcc
	global_store_dwordx4 v[14:15], v[10:13], off
	v_add_co_u32_e32 v14, vcc, s77, v46
	s_waitcnt lgkmcnt(6)
	v_cvt_pk_bf16_f32 v10, v30, v32
	s_waitcnt lgkmcnt(4)
	v_cvt_pk_bf16_f32 v11, v34, v36
	s_waitcnt lgkmcnt(2)
	v_cvt_pk_bf16_f32 v12, v38, v40
	s_waitcnt lgkmcnt(0)
	v_cvt_pk_bf16_f32 v13, v42, v44
	v_addc_co_u32_e32 v15, vcc, 0, v47, vcc
	global_store_dwordx4 v[14:15], v[10:13], off
	v_add_co_u32_e32 v14, vcc, s82, v46
	s_nop 0
	v_cvt_pk_bf16_f32 v10, v31, v33
	v_cvt_pk_bf16_f32 v11, v35, v37
	v_cvt_pk_bf16_f32 v12, v39, v41
	v_cvt_pk_bf16_f32 v13, v43, v45
	v_addc_co_u32_e32 v15, vcc, 0, v47, vcc
	global_store_dwordx4 v[14:15], v[10:13], off
	ds_read2_b32 v[14:15], v51 offset0:97 offset1:105
	ds_read2_b32 v[16:17], v51 offset0:162 offset1:170
	ds_read2_b32 v[18:19], v51 offset0:227 offset1:235
	ds_read2_b32 v[20:21], v56 offset0:36 offset1:44
	ds_read2_b32 v[22:23], v56 offset0:101 offset1:109
	ds_read2_b32 v[24:25], v56 offset0:166 offset1:174
	ds_read2_b32 v[26:27], v56 offset0:231 offset1:239
	ds_read2_b32 v[28:29], v51 offset0:32 offset1:40
	ds_read2_b32 v[30:31], v51 offset0:48 offset1:56
	ds_read2_b32 v[32:33], v51 offset0:113 offset1:121
	ds_read2_b32 v[34:35], v51 offset0:178 offset1:186
	ds_read2_b32 v[36:37], v51 offset0:243 offset1:251
	ds_read2_b32 v[38:39], v56 offset0:52 offset1:60
	ds_read2_b32 v[40:41], v56 offset0:117 offset1:125
	ds_read2_b32 v[42:43], v56 offset0:182 offset1:190
	ds_read2_b32 v[44:45], v56 offset0:247 offset1:255
	v_add_co_u32_e32 v56, vcc, s80, v46
	s_mov_b32 s22, 0x14000
	s_nop 0
	v_addc_co_u32_e32 v57, vcc, 0, v47, vcc
	s_waitcnt lgkmcnt(8)
	v_cvt_pk_bf16_f32 v10, v28, v14
	v_cvt_pk_bf16_f32 v11, v16, v18
	v_cvt_pk_bf16_f32 v12, v20, v22
	v_cvt_pk_bf16_f32 v13, v24, v26
	v_add_co_u32_e32 v14, vcc, s22, v46
	global_store_dwordx4 v[56:57], v[10:13], off
	s_nop 1
	v_cvt_pk_bf16_f32 v10, v29, v15
	v_cvt_pk_bf16_f32 v11, v17, v19
	v_cvt_pk_bf16_f32 v12, v21, v23
	v_cvt_pk_bf16_f32 v13, v25, v27
	v_addc_co_u32_e32 v15, vcc, 0, v47, vcc
	global_store_dwordx4 v[14:15], v[10:13], off
	v_add_co_u32_e32 v14, vcc, s83, v46
	s_waitcnt lgkmcnt(6)
	v_cvt_pk_bf16_f32 v10, v30, v32
	s_waitcnt lgkmcnt(4)
	v_cvt_pk_bf16_f32 v11, v34, v36
	s_waitcnt lgkmcnt(2)
	v_cvt_pk_bf16_f32 v12, v38, v40
	s_waitcnt lgkmcnt(0)
	v_cvt_pk_bf16_f32 v13, v42, v44
	v_addc_co_u32_e32 v15, vcc, 0, v47, vcc
	global_store_dwordx4 v[14:15], v[10:13], off
	v_add_co_u32_e32 v14, vcc, 0x1c000, v46
	s_nop 0
	v_cvt_pk_bf16_f32 v10, v31, v33
	v_cvt_pk_bf16_f32 v11, v35, v37
	v_cvt_pk_bf16_f32 v12, v39, v41
	v_cvt_pk_bf16_f32 v13, v43, v45
	v_addc_co_u32_e32 v15, vcc, 0, v47, vcc
	global_store_dwordx4 v[14:15], v[10:13], off

.LBB0_1026:
	s_andn2_saveexec_b64 s[18:19], s[18:19]
	s_cbranch_execz .LBB0_1028
	v_add_u32_e32 v10, 0xfffff930, v3
	v_lshrrev_b32_e32 v130, 7, v10
	v_lshl_add_u64 v[10:11], s[6:7], 0, v[130:131]
	v_readlane_b32 s40, v251, 35
	v_and_b32_e32 v84, 0x1c0, v52
	v_lshlrev_b64 v[10:11], 21, v[10:11]
	v_readlane_b32 s50, v251, 45
	v_readlane_b32 s51, v251, 46
	v_and_b32_e32 v85, 0x3c0, v55
	v_or_b32_e32 v13, v84, v9
	v_lshl_add_u64 v[10:11], s[50:51], 0, v[10:11]
	v_lshlrev_b64 v[46:47], 20, v[130:131]
	v_or_b32_e32 v12, v85, v48
	v_lshlrev_b32_e32 v130, 12, v13
	v_lshl_add_u64 v[10:11], v[10:11], 0, v[130:131]
	v_lshlrev_b32_e32 v130, 2, v12
	v_lshl_add_u64 v[76:77], v[10:11], 0, v[130:131]
	s_waitcnt lgkmcnt(0)
	v_add_co_u32_e32 v14, vcc, s88, v76
	s_mov_b32 s21, 0x8000
	s_nop 0
	v_addc_co_u32_e32 v15, vcc, 0, v77, vcc
	v_add_co_u32_e32 v18, vcc, s21, v76
	s_mov_b32 s22, 0xc000
	s_nop 0
	v_addc_co_u32_e32 v19, vcc, 0, v77, vcc
	v_add_co_u32_e32 v22, vcc, s22, v76
	s_mov_b32 s20, 0x14000
	s_nop 0
	v_addc_co_u32_e32 v23, vcc, 0, v77, vcc
	v_add_co_u32_e32 v26, vcc, s80, v76
	global_load_dwordx4 v[10:13], v[76:77], off nt
	s_nop 0
	global_load_dwordx4 v[14:17], v[14:15], off nt
	v_addc_co_u32_e32 v27, vcc, 0, v77, vcc
	v_add_co_u32_e32 v30, vcc, s20, v76
	s_mov_b32 s20, 0x1c000
	s_nop 0
	v_addc_co_u32_e32 v31, vcc, 0, v77, vcc
	v_add_co_u32_e32 v34, vcc, s83, v76
	global_load_dwordx4 v[18:21], v[18:19], off nt
	s_nop 0
	global_load_dwordx4 v[22:25], v[22:23], off nt
	v_addc_co_u32_e32 v35, vcc, 0, v77, vcc
	v_add_co_u32_e32 v38, vcc, s20, v76
	s_mov_b32 s20, 0x20000
	s_nop 0
	v_addc_co_u32_e32 v39, vcc, 0, v77, vcc
	v_add_co_u32_e32 v42, vcc, s20, v76
	s_mov_b32 s20, 0x24000
	s_nop 0
	v_addc_co_u32_e32 v43, vcc, 0, v77, vcc
	v_add_co_u32_e32 v56, vcc, s20, v76
	s_mov_b32 s20, 0x28000
	s_nop 0
	v_addc_co_u32_e32 v57, vcc, 0, v77, vcc
	v_add_co_u32_e32 v60, vcc, s20, v76
	s_mov_b32 s20, 0x2c000
	s_nop 0
	v_addc_co_u32_e32 v61, vcc, 0, v77, vcc
	v_add_co_u32_e32 v64, vcc, s20, v76
	s_mov_b32 s20, 0x30000
	s_nop 0
	v_addc_co_u32_e32 v65, vcc, 0, v77, vcc
	v_add_co_u32_e32 v68, vcc, s20, v76
	s_mov_b32 s20, 0x34000
	s_nop 0
	v_addc_co_u32_e32 v69, vcc, 0, v77, vcc
	v_add_co_u32_e32 v72, vcc, s20, v76
	s_mov_b32 s20, 0x38000
	s_nop 0
	v_addc_co_u32_e32 v73, vcc, 0, v77, vcc
	v_add_co_u32_e32 v78, vcc, s20, v76
	s_mov_b32 s20, 0x3c000
	s_nop 0
	v_addc_co_u32_e32 v79, vcc, 0, v77, vcc
	v_add_co_u32_e32 v80, vcc, s20, v76
	global_load_dwordx4 v[26:29], v[26:27], off nt
	s_nop 0
	global_load_dwordx4 v[30:33], v[30:31], off nt
	v_addc_co_u32_e32 v81, vcc, 0, v77, vcc
	global_load_dwordx4 v[34:37], v[34:35], off nt
	s_nop 0
	global_load_dwordx4 v[38:41], v[38:39], off nt
	s_nop 0
	global_load_dwordx4 v[42:45], v[42:43], off nt
	s_nop 0
	global_load_dwordx4 v[56:59], v[56:57], off nt
	s_nop 0
	global_load_dwordx4 v[60:63], v[60:61], off nt
	s_nop 0
	global_load_dwordx4 v[64:67], v[64:65], off nt
	s_nop 0
	global_load_dwordx4 v[68:71], v[68:69], off nt
	s_nop 0
	global_load_dwordx4 v[72:75], v[72:73], off nt
	s_nop 0
	global_load_dwordx4 v[76:79], v[78:79], off nt
	s_nop 0
	global_load_dwordx4 v[80:83], v[80:81], off nt
	v_readlane_b32 s54, v251, 49
	s_movk_i32 s54, 0x1000
	v_readlane_b32 s41, v251, 36
	v_readlane_b32 s42, v251, 37
	v_readlane_b32 s43, v251, 38
	v_readlane_b32 s44, v251, 39
	v_readlane_b32 s45, v251, 40
	v_readlane_b32 s46, v251, 41
	v_readlane_b32 s47, v251, 42
	v_readlane_b32 s48, v251, 43
	v_readlane_b32 s49, v251, 44
	v_readlane_b32 s52, v251, 47
	v_readlane_b32 s53, v251, 48
	v_readlane_b32 s55, v251, 50
	v_lshl_add_u64 v[46:47], s[12:13], 0, v[46:47]
	s_waitcnt vmcnt(0)
	ds_write2_b32 v49, v10, v11 offset1:1
	ds_write2_b32 v49, v12, v13 offset0:2 offset1:3
	v_add_u32_e32 v10, 0x410, v49
	ds_write2_b32 v10, v14, v15 offset1:1
	v_add_u32_e32 v10, 0x418, v49
	ds_write2_b32 v10, v16, v17 offset1:1
	v_add_u32_e32 v10, 0x820, v49
	ds_write2_b32 v10, v18, v19 offset1:1
	v_add_u32_e32 v10, 0x828, v49
	ds_write2_b32 v10, v20, v21 offset1:1
	v_add_u32_e32 v10, 0xc30, v49
	ds_write2_b32 v10, v22, v23 offset1:1
	v_add_u32_e32 v10, 0xc38, v49
	ds_write2_b32 v10, v24, v25 offset1:1
	v_add_u32_e32 v10, 0x1040, v49
	ds_write2_b32 v10, v26, v27 offset1:1
	v_add_u32_e32 v10, 0x1048, v49
	ds_write2_b32 v10, v28, v29 offset1:1
	v_add_u32_e32 v10, 0x1450, v49
	ds_write2_b32 v10, v30, v31 offset1:1
	v_add_u32_e32 v10, 0x1458, v49
	ds_write2_b32 v10, v32, v33 offset1:1
	v_add_u32_e32 v10, 0x1860, v49
	ds_write2_b32 v10, v34, v35 offset1:1
	v_add_u32_e32 v10, 0x1868, v49
	ds_write2_b32 v10, v36, v37 offset1:1
	v_add_u32_e32 v10, 0x1c70, v49
	ds_write2_b32 v10, v38, v39 offset1:1
	v_add_u32_e32 v10, 0x1c78, v49
	ds_write2_b32 v10, v40, v41 offset1:1
	v_add_u32_e32 v10, 0x2080, v49
	ds_write2_b32 v10, v42, v43 offset1:1
	v_add_u32_e32 v10, 0x2088, v49
	ds_write2_b32 v10, v44, v45 offset1:1
	v_add_u32_e32 v10, 0x2490, v49
	ds_write2_b32 v10, v56, v57 offset1:1
	v_add_u32_e32 v10, 0x2498, v49
	ds_write2_b32 v10, v58, v59 offset1:1
	v_add_u32_e32 v10, 0x28a0, v49
	ds_write2_b32 v10, v60, v61 offset1:1
	v_add_u32_e32 v10, 0x28a8, v49
	ds_write2_b32 v10, v62, v63 offset1:1
	v_add_u32_e32 v10, 0x2cb0, v49
	ds_write2_b32 v10, v64, v65 offset1:1
	v_add_u32_e32 v10, 0x2cb8, v49
	ds_write2_b32 v10, v66, v67 offset1:1
	v_add_u32_e32 v10, 0x30c0, v49
	ds_write2_b32 v10, v68, v69 offset1:1
	v_add_u32_e32 v10, 0x30c8, v49
	ds_write2_b32 v10, v70, v71 offset1:1
	v_add_u32_e32 v10, 0x34d0, v49
	ds_write2_b32 v10, v72, v73 offset1:1
	v_add_u32_e32 v10, 0x34d8, v49
	ds_write2_b32 v10, v74, v75 offset1:1
	v_add_u32_e32 v10, 0x38e0, v49
	ds_write2_b32 v10, v76, v77 offset1:1
	v_add_u32_e32 v10, 0x38e8, v49
	ds_write2_b32 v10, v78, v79 offset1:1
	v_add_u32_e32 v10, 0x3cf0, v49
	ds_write2_b32 v10, v80, v81 offset1:1
	v_add_u32_e32 v10, 0x3cf8, v49
	ds_write2_b32 v10, v82, v83 offset1:1
	v_add_u32_e32 v57, 0x400, v51
	ds_read2_b32 v[14:15], v51 offset0:65 offset1:73
	ds_read2_b32 v[16:17], v51 offset0:130 offset1:138
	ds_read2_b32 v[18:19], v51 offset0:195 offset1:203
	ds_read2_b32 v[20:21], v57 offset0:4 offset1:12
	ds_read2_b32 v[22:23], v57 offset0:69 offset1:77
	ds_read2_b32 v[24:25], v57 offset0:134 offset1:142
	ds_read2_b32 v[26:27], v57 offset0:199 offset1:207
	ds_read2_b32 v[28:29], v51 offset1:8
	ds_read2_b32 v[30:31], v51 offset0:16 offset1:24
	ds_read2_b32 v[32:33], v51 offset0:81 offset1:89
	ds_read2_b32 v[34:35], v51 offset0:146 offset1:154
	ds_read2_b32 v[36:37], v51 offset0:211 offset1:219
	ds_read2_b32 v[38:39], v57 offset0:20 offset1:28
	ds_read2_b32 v[40:41], v57 offset0:85 offset1:93
	ds_read2_b32 v[42:43], v57 offset0:150 offset1:158
	ds_read2_b32 v[44:45], v57 offset0:215 offset1:223
	v_lshlrev_b32_e32 v130, 1, v84
	v_lshl_add_u64 v[10:11], v[46:47], 0, v[130:131]
	v_lshlrev_b32_e32 v130, 1, v2
	v_or_b32_e32 v56, v85, v50
	v_lshl_add_u64 v[46:47], v[10:11], 0, v[130:131]
	v_lshlrev_b32_e32 v130, 10, v56
	v_lshl_add_u64 v[46:47], v[46:47], 0, v[130:131]
	s_waitcnt lgkmcnt(8)
	v_cvt_pk_bf16_f32 v10, v28, v14
	v_cvt_pk_bf16_f32 v11, v16, v18
	v_cvt_pk_bf16_f32 v12, v20, v22
	v_cvt_pk_bf16_f32 v13, v24, v26
	v_add_co_u32_e32 v14, vcc, s76, v46
	global_store_dwordx4 v[46:47], v[10:13], off
	s_nop 1
	v_cvt_pk_bf16_f32 v10, v29, v15
	v_cvt_pk_bf16_f32 v11, v17, v19
	v_cvt_pk_bf16_f32 v12, v21, v23
	v_cvt_pk_bf16_f32 v13, v25, v27
	v_addc_co_u32_e32 v15, vcc, 0, v47, vcc
	global_store_dwordx4 v[14:15], v[10:13], off
	v_add_co_u32_e32 v14, vcc, s88, v46
	s_waitcnt lgkmcnt(6)
	v_cvt_pk_bf16_f32 v10, v30, v32
	s_waitcnt lgkmcnt(4)
	v_cvt_pk_bf16_f32 v11, v34, v36
	s_waitcnt lgkmcnt(2)
	v_cvt_pk_bf16_f32 v12, v38, v40
	s_waitcnt lgkmcnt(0)
	v_cvt_pk_bf16_f32 v13, v42, v44
	v_addc_co_u32_e32 v15, vcc, 0, v47, vcc
	global_store_dwordx4 v[14:15], v[10:13], off
	v_add_co_u32_e32 v14, vcc, s75, v46
	s_nop 0
	v_cvt_pk_bf16_f32 v10, v31, v33
	v_cvt_pk_bf16_f32 v11, v35, v37
	v_cvt_pk_bf16_f32 v12, v39, v41
	v_cvt_pk_bf16_f32 v13, v43, v45
	v_addc_co_u32_e32 v15, vcc, 0, v47, vcc
	global_store_dwordx4 v[14:15], v[10:13], off
	ds_read2_b32 v[14:15], v51 offset0:97 offset1:105
	ds_read2_b32 v[16:17], v51 offset0:162 offset1:170
	ds_read2_b32 v[18:19], v51 offset0:227 offset1:235
	ds_read2_b32 v[20:21], v57 offset0:36 offset1:44
	ds_read2_b32 v[22:23], v57 offset0:101 offset1:109
	ds_read2_b32 v[24:25], v57 offset0:166 offset1:174
	ds_read2_b32 v[26:27], v57 offset0:231 offset1:239
	ds_read2_b32 v[28:29], v51 offset0:32 offset1:40
	ds_read2_b32 v[30:31], v51 offset0:48 offset1:56
	ds_read2_b32 v[32:33], v51 offset0:113 offset1:121
	ds_read2_b32 v[34:35], v51 offset0:178 offset1:186
	ds_read2_b32 v[36:37], v51 offset0:243 offset1:251
	ds_read2_b32 v[38:39], v57 offset0:52 offset1:60
	ds_read2_b32 v[40:41], v57 offset0:117 offset1:125
	ds_read2_b32 v[42:43], v57 offset0:182 offset1:190
	ds_read2_b32 v[44:45], v57 offset0:247 offset1:255
	v_add_co_u32_e32 v56, vcc, s21, v46
	s_mov_b32 s20, 0xa000
	s_nop 0
	v_addc_co_u32_e32 v57, vcc, 0, v47, vcc
	s_waitcnt lgkmcnt(8)
	v_cvt_pk_bf16_f32 v10, v28, v14
	v_cvt_pk_bf16_f32 v11, v16, v18
	v_cvt_pk_bf16_f32 v12, v20, v22
	v_cvt_pk_bf16_f32 v13, v24, v26
	v_add_co_u32_e32 v14, vcc, s20, v46
	global_store_dwordx4 v[56:57], v[10:13], off
	s_mov_b32 s77, 0x8000
	s_mov_b32 s82, 0xc000
	v_cvt_pk_bf16_f32 v10, v29, v15
	v_cvt_pk_bf16_f32 v11, v17, v19
	v_cvt_pk_bf16_f32 v12, v21, v23
	v_cvt_pk_bf16_f32 v13, v25, v27
	v_addc_co_u32_e32 v15, vcc, 0, v47, vcc
	global_store_dwordx4 v[14:15], v[10:13], off
	v_add_co_u32_e32 v14, vcc, s22, v46
	s_waitcnt lgkmcnt(6)
	v_cvt_pk_bf16_f32 v10, v30, v32
	s_waitcnt lgkmcnt(4)
	v_cvt_pk_bf16_f32 v11, v34, v36
	s_waitcnt lgkmcnt(2)
	v_cvt_pk_bf16_f32 v12, v38, v40
	s_waitcnt lgkmcnt(0)
	v_cvt_pk_bf16_f32 v13, v42, v44
	v_addc_co_u32_e32 v15, vcc, 0, v47, vcc
	global_store_dwordx4 v[14:15], v[10:13], off
	v_add_co_u32_e32 v14, vcc, 0xe000, v46
	s_nop 0
	v_cvt_pk_bf16_f32 v10, v31, v33
	v_cvt_pk_bf16_f32 v11, v35, v37
	v_cvt_pk_bf16_f32 v12, v39, v41
	v_cvt_pk_bf16_f32 v13, v43, v45
	v_addc_co_u32_e32 v15, vcc, 0, v47, vcc
	global_store_dwordx4 v[14:15], v[10:13], off

.LBB0_1029:
	s_andn2_saveexec_b64 s[18:19], s[0:1]
	s_cbranch_execz .LBB0_1018
	v_ashrrev_i32_e32 v10, 31, v3
	v_lshrrev_b32_e32 v10, 28, v10
	v_add_u32_e32 v10, v3, v10
	v_ashrrev_i32_e32 v84, 4, v10
	v_lshlrev_b32_e32 v85, 6, v84
	v_or_b32_e32 v12, v85, v48
	s_mov_b32 s0, 0xff93c000
	v_mad_u64_u32 v[10:11], s[0:1], v84, s0, v[8:9]
	v_cmp_gt_i32_e32 vcc, s33, v12
	v_ashrrev_i32_e32 v11, 31, v10
	v_lshl_add_u64 v[10:11], v[10:11], 2, s[14:15]
	v_cndmask_b32_e32 v12, 0, v12, vcc
	v_ashrrev_i32_e32 v13, 31, v12
	v_lshl_add_u64 v[46:47], v[12:13], 2, v[10:11]
	s_mov_b32 s0, 0x1b000
	s_waitcnt lgkmcnt(0)
	v_add_co_u32_e64 v14, s[0:1], s0, v46
	s_nop 1
	v_addc_co_u32_e64 v15, s[0:1], 0, v47, s[0:1]
	s_mov_b32 s0, 0x36000
	s_nop 0
	v_add_co_u32_e64 v18, s[0:1], s0, v46
	global_load_dwordx4 v[10:13], v[46:47], off nt
	s_nop 0
	global_load_dwordx4 v[14:17], v[14:15], off offset:256 nt
	v_addc_co_u32_e64 v19, s[0:1], 0, v47, s[0:1]
	s_mov_b32 s0, 0x51000
	s_nop 0
	v_add_co_u32_e64 v22, s[0:1], s0, v46
	s_nop 1
	v_addc_co_u32_e64 v23, s[0:1], 0, v47, s[0:1]
	s_mov_b32 s0, 0x6c000
	s_nop 0
	v_add_co_u32_e64 v26, s[0:1], s0, v46
	global_load_dwordx4 v[18:21], v[18:19], off offset:512 nt
	s_nop 0
	global_load_dwordx4 v[22:25], v[22:23], off offset:768 nt
	v_addc_co_u32_e64 v27, s[0:1], 0, v47, s[0:1]
	s_mov_b32 s0, 0x87000
	s_nop 0
	v_add_co_u32_e64 v30, s[0:1], s0, v46
	s_nop 1
	v_addc_co_u32_e64 v31, s[0:1], 0, v47, s[0:1]
	s_mov_b32 s0, 0xa2000
	s_nop 0
	v_add_co_u32_e64 v34, s[0:1], s0, v46
	global_load_dwordx4 v[26:29], v[26:27], off offset:1024 nt
	s_nop 0
	global_load_dwordx4 v[30:33], v[30:31], off offset:1280 nt
	v_addc_co_u32_e64 v35, s[0:1], 0, v47, s[0:1]
	s_mov_b32 s0, 0xbd000
	s_nop 0
	v_add_co_u32_e64 v38, s[0:1], s0, v46
	s_nop 1
	v_addc_co_u32_e64 v39, s[0:1], 0, v47, s[0:1]
	s_mov_b32 s0, 0xd8000
	s_nop 0
	v_add_co_u32_e64 v42, s[0:1], s0, v46
	global_load_dwordx4 v[34:37], v[34:35], off offset:1536 nt
	s_nop 0
	global_load_dwordx4 v[38:41], v[38:39], off offset:1792 nt
	v_addc_co_u32_e64 v43, s[0:1], 0, v47, s[0:1]
	s_mov_b32 s0, 0xf3000
	s_nop 0
	v_add_co_u32_e64 v56, s[0:1], s0, v46
	s_nop 1
	v_addc_co_u32_e64 v57, s[0:1], 0, v47, s[0:1]
	s_mov_b32 s0, 0x10e000
	s_nop 0
	v_add_co_u32_e64 v60, s[0:1], s0, v46
	global_load_dwordx4 v[42:45], v[42:43], off offset:2048 nt
	s_nop 0
	global_load_dwordx4 v[56:59], v[56:57], off offset:2304 nt
	v_addc_co_u32_e64 v61, s[0:1], 0, v47, s[0:1]
	s_mov_b32 s0, 0x129000
	s_nop 0
	v_add_co_u32_e64 v64, s[0:1], s0, v46
	s_nop 1
	v_addc_co_u32_e64 v65, s[0:1], 0, v47, s[0:1]
	s_mov_b32 s0, 0x144000
	s_nop 0
	v_add_co_u32_e64 v68, s[0:1], s0, v46
	global_load_dwordx4 v[60:63], v[60:61], off offset:2560 nt
	s_nop 0
	global_load_dwordx4 v[64:67], v[64:65], off offset:2816 nt
	v_addc_co_u32_e64 v69, s[0:1], 0, v47, s[0:1]
	s_mov_b32 s0, 0x15f000
	s_nop 0
	v_add_co_u32_e64 v72, s[0:1], s0, v46
	s_nop 1
	v_addc_co_u32_e64 v73, s[0:1], 0, v47, s[0:1]
	s_mov_b32 s0, 0x17a000
	s_nop 0
	v_add_co_u32_e64 v76, s[0:1], s0, v46
	global_load_dwordx4 v[68:71], v[68:69], off offset:3072 nt
	s_nop 0
	global_load_dwordx4 v[72:75], v[72:73], off offset:3328 nt
	v_addc_co_u32_e64 v77, s[0:1], 0, v47, s[0:1]
	s_mov_b32 s0, 0x195000
	s_nop 0
	v_add_co_u32_e64 v46, s[0:1], s0, v46
	s_nop 1
	v_addc_co_u32_e64 v47, s[0:1], 0, v47, s[0:1]
	global_load_dwordx4 v[76:79], v[76:77], off offset:3584 nt
	s_nop 0
	global_load_dwordx4 v[80:83], v[46:47], off offset:3840 nt
	v_lshlrev_b32_e32 v46, 10, v84
	v_sub_u32_e32 v84, v52, v46
	s_waitcnt vmcnt(0)
	v_cndmask_b32_e32 v10, 0, v10, vcc
	v_cndmask_b32_e32 v11, 0, v11, vcc
	ds_write2_b32 v49, v10, v11 offset1:1
	v_cndmask_b32_e32 v10, 0, v12, vcc
	v_cndmask_b32_e32 v11, 0, v13, vcc
	ds_write2_b32 v49, v10, v11 offset0:2 offset1:3
	v_cndmask_b32_e32 v10, 0, v14, vcc
	v_cndmask_b32_e32 v11, 0, v15, vcc
	v_add_u32_e32 v12, 0x410, v49
	ds_write2_b32 v12, v10, v11 offset1:1
	v_cndmask_b32_e32 v10, 0, v16, vcc
	v_cndmask_b32_e32 v11, 0, v17, vcc
	v_add_u32_e32 v12, 0x418, v49
	ds_write2_b32 v12, v10, v11 offset1:1
	v_cndmask_b32_e32 v10, 0, v18, vcc
	v_cndmask_b32_e32 v11, 0, v19, vcc
	v_add_u32_e32 v12, 0x820, v49
	ds_write2_b32 v12, v10, v11 offset1:1
	v_cndmask_b32_e32 v10, 0, v20, vcc
	v_cndmask_b32_e32 v11, 0, v21, vcc
	v_add_u32_e32 v12, 0x828, v49
	ds_write2_b32 v12, v10, v11 offset1:1
	v_cndmask_b32_e32 v10, 0, v22, vcc
	v_cndmask_b32_e32 v11, 0, v23, vcc
	v_add_u32_e32 v12, 0xc30, v49
	ds_write2_b32 v12, v10, v11 offset1:1
	v_cndmask_b32_e32 v10, 0, v24, vcc
	v_cndmask_b32_e32 v11, 0, v25, vcc
	v_add_u32_e32 v12, 0xc38, v49
	ds_write2_b32 v12, v10, v11 offset1:1
	v_cndmask_b32_e32 v10, 0, v26, vcc
	v_cndmask_b32_e32 v11, 0, v27, vcc
	v_add_u32_e32 v12, 0x1040, v49
	ds_write2_b32 v12, v10, v11 offset1:1
	v_cndmask_b32_e32 v10, 0, v28, vcc
	v_cndmask_b32_e32 v11, 0, v29, vcc
	v_add_u32_e32 v12, 0x1048, v49
	ds_write2_b32 v12, v10, v11 offset1:1
	v_cndmask_b32_e32 v10, 0, v30, vcc
	v_cndmask_b32_e32 v11, 0, v31, vcc
	v_add_u32_e32 v12, 0x1450, v49
	ds_write2_b32 v12, v10, v11 offset1:1
	v_cndmask_b32_e32 v10, 0, v32, vcc
	v_cndmask_b32_e32 v11, 0, v33, vcc
	v_add_u32_e32 v12, 0x1458, v49
	ds_write2_b32 v12, v10, v11 offset1:1
	v_cndmask_b32_e32 v10, 0, v34, vcc
	v_cndmask_b32_e32 v11, 0, v35, vcc
	v_add_u32_e32 v12, 0x1860, v49
	ds_write2_b32 v12, v10, v11 offset1:1
	v_cndmask_b32_e32 v10, 0, v36, vcc
	v_cndmask_b32_e32 v11, 0, v37, vcc
	v_add_u32_e32 v12, 0x1868, v49
	ds_write2_b32 v12, v10, v11 offset1:1
	v_cndmask_b32_e32 v10, 0, v38, vcc
	v_cndmask_b32_e32 v11, 0, v39, vcc
	v_add_u32_e32 v12, 0x1c70, v49
	ds_write2_b32 v12, v10, v11 offset1:1
	v_cndmask_b32_e32 v10, 0, v40, vcc
	v_cndmask_b32_e32 v11, 0, v41, vcc
	v_add_u32_e32 v12, 0x1c78, v49
	ds_write2_b32 v12, v10, v11 offset1:1
	v_cndmask_b32_e32 v10, 0, v42, vcc
	v_cndmask_b32_e32 v11, 0, v43, vcc
	v_add_u32_e32 v12, 0x2080, v49
	ds_write2_b32 v12, v10, v11 offset1:1
	v_cndmask_b32_e32 v10, 0, v44, vcc
	v_cndmask_b32_e32 v11, 0, v45, vcc
	v_add_u32_e32 v12, 0x2088, v49
	ds_write2_b32 v12, v10, v11 offset1:1
	v_cndmask_b32_e32 v10, 0, v56, vcc
	v_cndmask_b32_e32 v11, 0, v57, vcc
	v_add_u32_e32 v12, 0x2490, v49
	ds_write2_b32 v12, v10, v11 offset1:1
	v_cndmask_b32_e32 v10, 0, v58, vcc
	v_cndmask_b32_e32 v11, 0, v59, vcc
	v_add_u32_e32 v12, 0x2498, v49
	ds_write2_b32 v12, v10, v11 offset1:1
	v_cndmask_b32_e32 v10, 0, v60, vcc
	v_cndmask_b32_e32 v11, 0, v61, vcc
	v_add_u32_e32 v12, 0x28a0, v49
	ds_write2_b32 v12, v10, v11 offset1:1
	v_cndmask_b32_e32 v10, 0, v62, vcc
	v_cndmask_b32_e32 v11, 0, v63, vcc
	v_add_u32_e32 v12, 0x28a8, v49
	ds_write2_b32 v12, v10, v11 offset1:1
	v_cndmask_b32_e32 v10, 0, v64, vcc
	v_cndmask_b32_e32 v11, 0, v65, vcc
	v_add_u32_e32 v12, 0x2cb0, v49
	ds_write2_b32 v12, v10, v11 offset1:1
	v_cndmask_b32_e32 v10, 0, v66, vcc
	v_cndmask_b32_e32 v11, 0, v67, vcc
	v_add_u32_e32 v12, 0x2cb8, v49
	ds_write2_b32 v12, v10, v11 offset1:1
	v_cndmask_b32_e32 v10, 0, v68, vcc
	v_cndmask_b32_e32 v11, 0, v69, vcc
	v_add_u32_e32 v12, 0x30c0, v49
	ds_write2_b32 v12, v10, v11 offset1:1
	v_cndmask_b32_e32 v10, 0, v70, vcc
	v_cndmask_b32_e32 v11, 0, v71, vcc
	v_add_u32_e32 v12, 0x30c8, v49
	ds_write2_b32 v12, v10, v11 offset1:1
	v_cndmask_b32_e32 v10, 0, v72, vcc
	v_cndmask_b32_e32 v11, 0, v73, vcc
	v_add_u32_e32 v12, 0x34d0, v49
	ds_write2_b32 v12, v10, v11 offset1:1
	v_cndmask_b32_e32 v10, 0, v74, vcc
	v_cndmask_b32_e32 v11, 0, v75, vcc
	v_add_u32_e32 v12, 0x34d8, v49
	ds_write2_b32 v12, v10, v11 offset1:1
	v_cndmask_b32_e32 v10, 0, v76, vcc
	v_cndmask_b32_e32 v11, 0, v77, vcc
	v_add_u32_e32 v12, 0x38e0, v49
	ds_write2_b32 v12, v10, v11 offset1:1
	v_cndmask_b32_e32 v10, 0, v78, vcc
	v_cndmask_b32_e32 v11, 0, v79, vcc
	v_add_u32_e32 v12, 0x38e8, v49
	ds_write2_b32 v12, v10, v11 offset1:1
	v_cndmask_b32_e32 v10, 0, v80, vcc
	v_cndmask_b32_e32 v11, 0, v81, vcc
	v_add_u32_e32 v12, 0x3cf0, v49
	ds_write2_b32 v12, v10, v11 offset1:1
	v_cndmask_b32_e32 v10, 0, v82, vcc
	v_cndmask_b32_e32 v11, 0, v83, vcc
	v_add_u32_e32 v12, 0x3cf8, v49
	ds_write2_b32 v12, v10, v11 offset1:1
	v_add_u32_e32 v46, 0x400, v51
	ds_read2_b32 v[30:31], v51 offset1:8
	ds_read2_b32 v[32:33], v51 offset0:65 offset1:73
	ds_read2_b32 v[34:35], v51 offset0:130 offset1:138
	ds_read2_b32 v[36:37], v51 offset0:195 offset1:203
	ds_read2_b32 v[38:39], v46 offset0:4 offset1:12
	ds_read2_b32 v[40:41], v46 offset0:69 offset1:77
	ds_read2_b32 v[42:43], v46 offset0:134 offset1:142
	ds_read2_b32 v[44:45], v46 offset0:199 offset1:207
	ds_read2_b32 v[14:15], v51 offset0:16 offset1:24
	ds_read2_b32 v[16:17], v51 offset0:81 offset1:89
	ds_read2_b32 v[18:19], v51 offset0:146 offset1:154
	ds_read2_b32 v[20:21], v51 offset0:211 offset1:219
	ds_read2_b32 v[22:23], v46 offset0:20 offset1:28
	ds_read2_b32 v[24:25], v46 offset0:85 offset1:93
	ds_read2_b32 v[26:27], v46 offset0:150 offset1:158
	ds_read2_b32 v[28:29], v46 offset0:215 offset1:223
	v_or_b32_e32 v12, v85, v50
	v_ashrrev_i32_e32 v85, 31, v84
	v_lshl_add_u64 v[10:11], v[84:85], 1, v[6:7]
	v_cmp_gt_i32_e32 vcc, s33, v12
	s_and_saveexec_b64 s[0:1], vcc
	s_cbranch_execz .LBB0_1032
	v_ashrrev_i32_e32 v13, 31, v12
	v_lshlrev_b64 v[60:61], 11, v[12:13]
	s_waitcnt lgkmcnt(14)
	v_cvt_pk_bf16_f32 v56, v30, v32
	s_waitcnt lgkmcnt(12)
	v_cvt_pk_bf16_f32 v57, v34, v36
	s_waitcnt lgkmcnt(10)
	v_cvt_pk_bf16_f32 v58, v38, v40
	s_waitcnt lgkmcnt(8)
	v_cvt_pk_bf16_f32 v59, v42, v44
	v_lshl_add_u64 v[60:61], v[10:11], 0, v[60:61]
	global_store_dwordx4 v[60:61], v[56:59], off

.LBB0_1409:
	s_movk_i32 s0, 0x6cf
	v_cmp_lt_i32_e32 vcc, s0, v3
	s_and_saveexec_b64 s[0:1], vcc
	s_xor_b64 s[0:1], exec, s[0:1]
	s_cbranch_execz .LBB0_1419
	s_movk_i32 s18, 0x84f
	v_cmp_lt_u32_e32 vcc, s18, v3
	s_and_saveexec_b64 s[18:19], vcc
	s_xor_b64 s[18:19], exec, s[18:19]
	s_cbranch_execz .LBB0_1416
	s_movk_i32 s20, 0x94f
	v_cmp_lt_u32_e32 vcc, s20, v3
	s_and_saveexec_b64 s[20:21], vcc
	s_xor_b64 s[20:21], exec, s[20:21]
	s_cbranch_execz .LBB0_1413
	v_and_b32_e32 v84, 0x3c0, v52
	v_and_b32_e32 v130, 0x7800000, v54
	v_add_u32_e32 v85, 0xffffdac0, v53
	s_movk_i32 s22, 0x7c0
	v_or_b32_e32 v13, v84, v9
	v_lshl_add_u64 v[10:11], s[6:7], 0, v[130:131]
	v_lshl_add_u64 v[46:47], s[8:9], 0, v[130:131]
	v_and_or_b32 v12, v85, s22, v48
	v_lshlrev_b32_e32 v130, 13, v13
	v_lshl_add_u64 v[10:11], v[10:11], 0, v[130:131]
	v_lshlrev_b32_e32 v130, 2, v12
	v_lshl_add_u64 v[76:77], v[10:11], 0, v[130:131]
	s_waitcnt lgkmcnt(0)
	v_add_co_u32_e32 v14, vcc, 0x8000, v76
	s_mov_b32 s22, 0x20000
	s_nop 0
	v_addc_co_u32_e32 v15, vcc, 0, v77, vcc
	v_add_co_u32_e32 v18, vcc, 0x10000, v76
	global_load_dwordx4 v[10:13], v[76:77], off nt
	s_nop 0
	global_load_dwordx4 v[14:17], v[14:15], off nt
	v_addc_co_u32_e32 v19, vcc, 0, v77, vcc
	v_add_co_u32_e32 v22, vcc, 0x18000, v76
	s_nop 1
	v_addc_co_u32_e32 v23, vcc, 0, v77, vcc
	v_add_co_u32_e32 v26, vcc, s22, v76
	s_mov_b32 s22, 0x40000
	s_nop 0
	v_addc_co_u32_e32 v27, vcc, 0, v77, vcc
	v_add_co_u32_e32 v30, vcc, 0x28000, v76
	global_load_dwordx4 v[18:21], v[18:19], off nt
	s_nop 0
	global_load_dwordx4 v[22:25], v[22:23], off nt
	v_addc_co_u32_e32 v31, vcc, 0, v77, vcc
	v_add_co_u32_e32 v34, vcc, 0x30000, v76
	global_load_dwordx4 v[26:29], v[26:27], off nt
	s_nop 0
	global_load_dwordx4 v[30:33], v[30:31], off nt
	v_addc_co_u32_e32 v35, vcc, 0, v77, vcc
	v_add_co_u32_e32 v38, vcc, 0x38000, v76
	s_nop 1
	v_addc_co_u32_e32 v39, vcc, 0, v77, vcc
	v_add_co_u32_e32 v42, vcc, s22, v76
	global_load_dwordx4 v[34:37], v[34:35], off nt
	s_nop 0
	global_load_dwordx4 v[38:41], v[38:39], off nt
	v_addc_co_u32_e32 v43, vcc, 0, v77, vcc
	v_add_co_u32_e32 v56, vcc, 0x48000, v76
	s_nop 1
	v_addc_co_u32_e32 v57, vcc, 0, v77, vcc
	v_add_co_u32_e32 v60, vcc, 0x50000, v76
	global_load_dwordx4 v[42:45], v[42:43], off nt
	s_nop 0
	global_load_dwordx4 v[56:59], v[56:57], off nt
	v_addc_co_u32_e32 v61, vcc, 0, v77, vcc
	v_add_co_u32_e32 v64, vcc, 0x58000, v76
	s_nop 1
	v_addc_co_u32_e32 v65, vcc, 0, v77, vcc
	v_add_co_u32_e32 v68, vcc, 0x60000, v76
	global_load_dwordx4 v[60:63], v[60:61], off nt
	s_nop 0
	global_load_dwordx4 v[64:67], v[64:65], off nt
	v_addc_co_u32_e32 v69, vcc, 0, v77, vcc
	v_add_co_u32_e32 v72, vcc, 0x68000, v76
	s_nop 1
	v_addc_co_u32_e32 v73, vcc, 0, v77, vcc
	v_add_co_u32_e32 v78, vcc, 0x70000, v76
	global_load_dwordx4 v[68:71], v[68:69], off nt
	s_nop 0
	global_load_dwordx4 v[72:75], v[72:73], off nt
	v_addc_co_u32_e32 v79, vcc, 0, v77, vcc
	v_add_co_u32_e32 v80, vcc, 0x78000, v76
	s_nop 1
	v_addc_co_u32_e32 v81, vcc, 0, v77, vcc
	global_load_dwordx4 v[76:79], v[78:79], off nt
	s_nop 0
	global_load_dwordx4 v[80:83], v[80:81], off nt
	s_waitcnt vmcnt(0)
	ds_write2_b32 v49, v10, v11 offset1:1
	ds_write2_b32 v49, v12, v13 offset0:2 offset1:3
	v_add_u32_e32 v10, 0x410, v49
	ds_write2_b32 v10, v14, v15 offset1:1
	v_add_u32_e32 v10, 0x418, v49
	ds_write2_b32 v10, v16, v17 offset1:1
	v_add_u32_e32 v10, 0x820, v49
	ds_write2_b32 v10, v18, v19 offset1:1
	v_add_u32_e32 v10, 0x828, v49
	ds_write2_b32 v10, v20, v21 offset1:1
	v_add_u32_e32 v10, 0xc30, v49
	ds_write2_b32 v10, v22, v23 offset1:1
	v_add_u32_e32 v10, 0xc38, v49
	ds_write2_b32 v10, v24, v25 offset1:1
	v_add_u32_e32 v10, 0x1040, v49
	ds_write2_b32 v10, v26, v27 offset1:1
	v_add_u32_e32 v10, 0x1048, v49
	ds_write2_b32 v10, v28, v29 offset1:1
	v_add_u32_e32 v10, 0x1450, v49
	ds_write2_b32 v10, v30, v31 offset1:1
	v_add_u32_e32 v10, 0x1458, v49
	ds_write2_b32 v10, v32, v33 offset1:1
	v_add_u32_e32 v10, 0x1860, v49
	ds_write2_b32 v10, v34, v35 offset1:1
	v_add_u32_e32 v10, 0x1868, v49
	ds_write2_b32 v10, v36, v37 offset1:1
	v_add_u32_e32 v10, 0x1c70, v49
	ds_write2_b32 v10, v38, v39 offset1:1
	v_add_u32_e32 v10, 0x1c78, v49
	ds_write2_b32 v10, v40, v41 offset1:1
	v_add_u32_e32 v10, 0x2080, v49
	ds_write2_b32 v10, v42, v43 offset1:1
	v_add_u32_e32 v10, 0x2088, v49
	ds_write2_b32 v10, v44, v45 offset1:1
	v_add_u32_e32 v10, 0x2490, v49
	ds_write2_b32 v10, v56, v57 offset1:1
	v_add_u32_e32 v10, 0x2498, v49
	ds_write2_b32 v10, v58, v59 offset1:1
	v_add_u32_e32 v10, 0x28a0, v49
	ds_write2_b32 v10, v60, v61 offset1:1
	v_add_u32_e32 v10, 0x28a8, v49
	ds_write2_b32 v10, v62, v63 offset1:1
	v_add_u32_e32 v10, 0x2cb0, v49
	ds_write2_b32 v10, v64, v65 offset1:1
	v_add_u32_e32 v10, 0x2cb8, v49
	ds_write2_b32 v10, v66, v67 offset1:1
	v_add_u32_e32 v10, 0x30c0, v49
	ds_write2_b32 v10, v68, v69 offset1:1
	v_add_u32_e32 v10, 0x30c8, v49
	ds_write2_b32 v10, v70, v71 offset1:1
	v_add_u32_e32 v10, 0x34d0, v49
	ds_write2_b32 v10, v72, v73 offset1:1
	v_add_u32_e32 v10, 0x34d8, v49
	ds_write2_b32 v10, v74, v75 offset1:1
	v_add_u32_e32 v10, 0x38e0, v49
	ds_write2_b32 v10, v76, v77 offset1:1
	v_add_u32_e32 v10, 0x38e8, v49
	ds_write2_b32 v10, v78, v79 offset1:1
	v_add_u32_e32 v10, 0x3cf0, v49
	ds_write2_b32 v10, v80, v81 offset1:1
	v_add_u32_e32 v10, 0x3cf8, v49
	ds_write2_b32 v10, v82, v83 offset1:1
	v_add_u32_e32 v56, 0x400, v51
	ds_read2_b32 v[14:15], v51 offset0:65 offset1:73
	ds_read2_b32 v[16:17], v51 offset0:130 offset1:138
	ds_read2_b32 v[18:19], v51 offset0:195 offset1:203
	ds_read2_b32 v[20:21], v56 offset0:4 offset1:12
	ds_read2_b32 v[22:23], v56 offset0:69 offset1:77
	ds_read2_b32 v[24:25], v56 offset0:134 offset1:142
	ds_read2_b32 v[26:27], v56 offset0:199 offset1:207
	ds_read2_b32 v[28:29], v51 offset1:8
	ds_read2_b32 v[30:31], v51 offset0:16 offset1:24
	ds_read2_b32 v[32:33], v51 offset0:81 offset1:89
	ds_read2_b32 v[34:35], v51 offset0:146 offset1:154
	ds_read2_b32 v[36:37], v51 offset0:211 offset1:219
	ds_read2_b32 v[38:39], v56 offset0:20 offset1:28
	ds_read2_b32 v[40:41], v56 offset0:85 offset1:93
	ds_read2_b32 v[42:43], v56 offset0:150 offset1:158
	ds_read2_b32 v[44:45], v56 offset0:215 offset1:223
	v_lshlrev_b32_e32 v130, 1, v84
	v_lshl_add_u64 v[10:11], v[46:47], 0, v[130:131]
	v_lshlrev_b32_e32 v130, 1, v2
	v_lshl_add_u64 v[46:47], v[10:11], 0, v[130:131]
	v_lshlrev_b32_e32 v10, 1, v85
	v_and_b32_e32 v10, 0xf00, v10
	v_and_b32_e32 v11, 64, v85
	v_or3_b32 v57, v11, v10, v50
	v_lshlrev_b32_e32 v130, 11, v57
	v_lshl_add_u64 v[46:47], v[46:47], 0, v[130:131]
	s_waitcnt lgkmcnt(8)
	v_cvt_pk_bf16_f32 v10, v28, v14
	v_cvt_pk_bf16_f32 v11, v16, v18
	v_cvt_pk_bf16_f32 v12, v20, v22
	v_cvt_pk_bf16_f32 v13, v24, v26
	v_add_co_u32_e32 v14, vcc, s88, v46
	global_store_dwordx4 v[46:47], v[10:13], off
	s_nop 1
	v_cvt_pk_bf16_f32 v10, v29, v15
	v_cvt_pk_bf16_f32 v11, v17, v19
	v_cvt_pk_bf16_f32 v12, v21, v23
	v_cvt_pk_bf16_f32 v13, v25, v27
	v_addc_co_u32_e32 v15, vcc, 0, v47, vcc
	global_store_dwordx4 v[14:15], v[10:13], off
	v_add_co_u32_e32 v14, vcc, s77, v46
	s_waitcnt lgkmcnt(6)
	v_cvt_pk_bf16_f32 v10, v30, v32
	s_waitcnt lgkmcnt(4)
	v_cvt_pk_bf16_f32 v11, v34, v36
	s_waitcnt lgkmcnt(2)
	v_cvt_pk_bf16_f32 v12, v38, v40
	s_waitcnt lgkmcnt(0)
	v_cvt_pk_bf16_f32 v13, v42, v44
	v_addc_co_u32_e32 v15, vcc, 0, v47, vcc
	global_store_dwordx4 v[14:15], v[10:13], off
	v_add_co_u32_e32 v14, vcc, s82, v46
	s_nop 0
	v_cvt_pk_bf16_f32 v10, v31, v33
	v_cvt_pk_bf16_f32 v11, v35, v37
	v_cvt_pk_bf16_f32 v12, v39, v41
	v_cvt_pk_bf16_f32 v13, v43, v45
	v_addc_co_u32_e32 v15, vcc, 0, v47, vcc
	global_store_dwordx4 v[14:15], v[10:13], off
	ds_read2_b32 v[14:15], v51 offset0:97 offset1:105
	ds_read2_b32 v[16:17], v51 offset0:162 offset1:170
	ds_read2_b32 v[18:19], v51 offset0:227 offset1:235
	ds_read2_b32 v[20:21], v56 offset0:36 offset1:44
	ds_read2_b32 v[22:23], v56 offset0:101 offset1:109
	ds_read2_b32 v[24:25], v56 offset0:166 offset1:174
	ds_read2_b32 v[26:27], v56 offset0:231 offset1:239
	ds_read2_b32 v[28:29], v51 offset0:32 offset1:40
	ds_read2_b32 v[30:31], v51 offset0:48 offset1:56
	ds_read2_b32 v[32:33], v51 offset0:113 offset1:121
	ds_read2_b32 v[34:35], v51 offset0:178 offset1:186
	ds_read2_b32 v[36:37], v51 offset0:243 offset1:251
	ds_read2_b32 v[38:39], v56 offset0:52 offset1:60
	ds_read2_b32 v[40:41], v56 offset0:117 offset1:125
	ds_read2_b32 v[42:43], v56 offset0:182 offset1:190
	ds_read2_b32 v[44:45], v56 offset0:247 offset1:255
	v_add_co_u32_e32 v56, vcc, s80, v46
	s_mov_b32 s22, 0x14000
	s_nop 0
	v_addc_co_u32_e32 v57, vcc, 0, v47, vcc
	s_waitcnt lgkmcnt(8)
	v_cvt_pk_bf16_f32 v10, v28, v14
	v_cvt_pk_bf16_f32 v11, v16, v18
	v_cvt_pk_bf16_f32 v12, v20, v22
	v_cvt_pk_bf16_f32 v13, v24, v26
	v_add_co_u32_e32 v14, vcc, s22, v46
	global_store_dwordx4 v[56:57], v[10:13], off
	s_nop 1
	v_cvt_pk_bf16_f32 v10, v29, v15
	v_cvt_pk_bf16_f32 v11, v17, v19
	v_cvt_pk_bf16_f32 v12, v21, v23
	v_cvt_pk_bf16_f32 v13, v25, v27
	v_addc_co_u32_e32 v15, vcc, 0, v47, vcc
	global_store_dwordx4 v[14:15], v[10:13], off
	v_add_co_u32_e32 v14, vcc, s83, v46
	s_waitcnt lgkmcnt(6)
	v_cvt_pk_bf16_f32 v10, v30, v32
	s_waitcnt lgkmcnt(4)
	v_cvt_pk_bf16_f32 v11, v34, v36
	s_waitcnt lgkmcnt(2)
	v_cvt_pk_bf16_f32 v12, v38, v40
	s_waitcnt lgkmcnt(0)
	v_cvt_pk_bf16_f32 v13, v42, v44
	v_addc_co_u32_e32 v15, vcc, 0, v47, vcc
	global_store_dwordx4 v[14:15], v[10:13], off
	v_add_co_u32_e32 v14, vcc, 0x1c000, v46
	s_nop 0
	v_cvt_pk_bf16_f32 v10, v31, v33
	v_cvt_pk_bf16_f32 v11, v35, v37
	v_cvt_pk_bf16_f32 v12, v39, v41
	v_cvt_pk_bf16_f32 v13, v43, v45
	v_addc_co_u32_e32 v15, vcc, 0, v47, vcc
	global_store_dwordx4 v[14:15], v[10:13], off
.LBB0_1413:
	s_andn2_saveexec_b64 s[20:21], s[20:21]
	s_cbranch_execz .LBB0_1415
	v_and_b32_e32 v84, 0x3c0, v52
	v_and_b32_e32 v10, 0x3fc0, v53
	v_or_b32_e32 v11, v84, v9
	v_add_u32_e32 v85, 0xffffdec0, v10
	v_lshlrev_b32_e32 v130, 12, v11
	v_or_b32_e32 v10, v85, v48
	v_lshl_add_u64 v[12:13], s[10:11], 0, v[130:131]
	v_mov_b32_e32 v11, v131
	v_lshl_add_u64 v[46:47], v[10:11], 2, v[12:13]
	s_waitcnt lgkmcnt(0)
	v_add_co_u32_e32 v14, vcc, 0x4000, v46
	s_mov_b32 s22, 0x20000
	s_nop 0
	v_addc_co_u32_e32 v15, vcc, 0, v47, vcc
	v_add_co_u32_e32 v18, vcc, 0x8000, v46
	global_load_dwordx4 v[10:13], v[46:47], off nt
	s_nop 0
	global_load_dwordx4 v[14:17], v[14:15], off nt
	v_addc_co_u32_e32 v19, vcc, 0, v47, vcc
	v_add_co_u32_e32 v22, vcc, 0xc000, v46
	s_nop 1
	v_addc_co_u32_e32 v23, vcc, 0, v47, vcc
	v_add_co_u32_e32 v26, vcc, 0x10000, v46
	global_load_dwordx4 v[18:21], v[18:19], off nt
	s_nop 0
	global_load_dwordx4 v[22:25], v[22:23], off nt
	v_addc_co_u32_e32 v27, vcc, 0, v47, vcc
	v_add_co_u32_e32 v30, vcc, 0x14000, v46
	s_nop 1
	v_addc_co_u32_e32 v31, vcc, 0, v47, vcc
	v_add_co_u32_e32 v34, vcc, 0x18000, v46
	global_load_dwordx4 v[26:29], v[26:27], off nt
	s_nop 0
	global_load_dwordx4 v[30:33], v[30:31], off nt
	v_addc_co_u32_e32 v35, vcc, 0, v47, vcc
	v_add_co_u32_e32 v38, vcc, 0x1c000, v46
	s_nop 1
	v_addc_co_u32_e32 v39, vcc, 0, v47, vcc
	v_add_co_u32_e32 v42, vcc, s22, v46
	global_load_dwordx4 v[34:37], v[34:35], off nt
	s_nop 0
	global_load_dwordx4 v[38:41], v[38:39], off nt
	v_addc_co_u32_e32 v43, vcc, 0, v47, vcc
	v_add_co_u32_e32 v56, vcc, 0x24000, v46
	s_nop 1
	v_addc_co_u32_e32 v57, vcc, 0, v47, vcc
	v_add_co_u32_e32 v60, vcc, 0x28000, v46
	global_load_dwordx4 v[42:45], v[42:43], off nt
	s_nop 0
	global_load_dwordx4 v[56:59], v[56:57], off nt
	v_addc_co_u32_e32 v61, vcc, 0, v47, vcc
	v_add_co_u32_e32 v64, vcc, 0x2c000, v46
	s_nop 1
	v_addc_co_u32_e32 v65, vcc, 0, v47, vcc
	v_add_co_u32_e32 v68, vcc, 0x30000, v46
	global_load_dwordx4 v[60:63], v[60:61], off nt
	s_nop 0
	global_load_dwordx4 v[64:67], v[64:65], off nt
	v_addc_co_u32_e32 v69, vcc, 0, v47, vcc
	v_add_co_u32_e32 v72, vcc, 0x34000, v46
	s_nop 1
	v_addc_co_u32_e32 v73, vcc, 0, v47, vcc
	v_add_co_u32_e32 v76, vcc, 0x38000, v46
	global_load_dwordx4 v[68:71], v[68:69], off nt
	s_nop 0
	global_load_dwordx4 v[72:75], v[72:73], off nt
	v_addc_co_u32_e32 v77, vcc, 0, v47, vcc
	v_add_co_u32_e32 v46, vcc, 0x3c000, v46
	s_nop 1
	v_addc_co_u32_e32 v47, vcc, 0, v47, vcc
	global_load_dwordx4 v[76:79], v[76:77], off nt
	s_nop 0
	global_load_dwordx4 v[80:83], v[46:47], off nt
	s_waitcnt vmcnt(0)
	ds_write2_b32 v49, v10, v11 offset1:1
	ds_write2_b32 v49, v12, v13 offset0:2 offset1:3
	v_add_u32_e32 v10, 0x410, v49
	ds_write2_b32 v10, v14, v15 offset1:1
	v_add_u32_e32 v10, 0x418, v49
	ds_write2_b32 v10, v16, v17 offset1:1
	v_add_u32_e32 v10, 0x820, v49
	ds_write2_b32 v10, v18, v19 offset1:1
	v_add_u32_e32 v10, 0x828, v49
	ds_write2_b32 v10, v20, v21 offset1:1
	v_add_u32_e32 v10, 0xc30, v49
	ds_write2_b32 v10, v22, v23 offset1:1
	v_add_u32_e32 v10, 0xc38, v49
	ds_write2_b32 v10, v24, v25 offset1:1
	v_add_u32_e32 v10, 0x1040, v49
	ds_write2_b32 v10, v26, v27 offset1:1
	v_add_u32_e32 v10, 0x1048, v49
	ds_write2_b32 v10, v28, v29 offset1:1
	v_add_u32_e32 v10, 0x1450, v49
	ds_write2_b32 v10, v30, v31 offset1:1
	v_add_u32_e32 v10, 0x1458, v49
	ds_write2_b32 v10, v32, v33 offset1:1
	v_add_u32_e32 v10, 0x1860, v49
	ds_write2_b32 v10, v34, v35 offset1:1
	v_add_u32_e32 v10, 0x1868, v49
	ds_write2_b32 v10, v36, v37 offset1:1
	v_add_u32_e32 v10, 0x1c70, v49
	ds_write2_b32 v10, v38, v39 offset1:1
	v_add_u32_e32 v10, 0x1c78, v49
	ds_write2_b32 v10, v40, v41 offset1:1
	v_add_u32_e32 v10, 0x2080, v49
	ds_write2_b32 v10, v42, v43 offset1:1
	v_add_u32_e32 v10, 0x2088, v49
	ds_write2_b32 v10, v44, v45 offset1:1
	v_add_u32_e32 v10, 0x2490, v49
	ds_write2_b32 v10, v56, v57 offset1:1
	v_add_u32_e32 v10, 0x2498, v49
	ds_write2_b32 v10, v58, v59 offset1:1
	v_add_u32_e32 v10, 0x28a0, v49
	ds_write2_b32 v10, v60, v61 offset1:1
	v_add_u32_e32 v10, 0x28a8, v49
	ds_write2_b32 v10, v62, v63 offset1:1
	v_add_u32_e32 v10, 0x2cb0, v49
	ds_write2_b32 v10, v64, v65 offset1:1
	v_add_u32_e32 v10, 0x2cb8, v49
	ds_write2_b32 v10, v66, v67 offset1:1
	v_add_u32_e32 v10, 0x30c0, v49
	ds_write2_b32 v10, v68, v69 offset1:1
	v_add_u32_e32 v10, 0x30c8, v49
	ds_write2_b32 v10, v70, v71 offset1:1
	v_add_u32_e32 v10, 0x34d0, v49
	ds_write2_b32 v10, v72, v73 offset1:1
	v_add_u32_e32 v10, 0x34d8, v49
	ds_write2_b32 v10, v74, v75 offset1:1
	v_add_u32_e32 v10, 0x38e0, v49
	ds_write2_b32 v10, v76, v77 offset1:1
	v_add_u32_e32 v10, 0x38e8, v49
	ds_write2_b32 v10, v78, v79 offset1:1
	v_add_u32_e32 v10, 0x3cf0, v49
	ds_write2_b32 v10, v80, v81 offset1:1
	v_add_u32_e32 v10, 0x3cf8, v49
	ds_write2_b32 v10, v82, v83 offset1:1
	v_add_u32_e32 v56, 0x400, v51
	ds_read2_b32 v[14:15], v51 offset0:65 offset1:73
	ds_read2_b32 v[16:17], v51 offset0:130 offset1:138
	ds_read2_b32 v[18:19], v51 offset0:195 offset1:203
	ds_read2_b32 v[20:21], v56 offset0:4 offset1:12
	ds_read2_b32 v[22:23], v56 offset0:69 offset1:77
	ds_read2_b32 v[24:25], v56 offset0:134 offset1:142
	ds_read2_b32 v[26:27], v56 offset0:199 offset1:207
	ds_read2_b32 v[28:29], v51 offset1:8
	ds_read2_b32 v[30:31], v51 offset0:16 offset1:24
	ds_read2_b32 v[32:33], v51 offset0:81 offset1:89
	ds_read2_b32 v[34:35], v51 offset0:146 offset1:154
	ds_read2_b32 v[36:37], v51 offset0:211 offset1:219
	ds_read2_b32 v[38:39], v56 offset0:20 offset1:28
	ds_read2_b32 v[40:41], v56 offset0:85 offset1:93
	ds_read2_b32 v[42:43], v56 offset0:150 offset1:158
	ds_read2_b32 v[44:45], v56 offset0:215 offset1:223
	v_lshlrev_b32_e32 v130, 1, v84
	v_or_b32_e32 v57, v85, v50
	v_lshl_add_u64 v[46:47], v[4:5], 0, v[130:131]
	v_lshlrev_b32_e32 v130, 11, v57
	v_lshl_add_u64 v[46:47], v[46:47], 0, v[130:131]
	s_waitcnt lgkmcnt(8)
	v_cvt_pk_bf16_f32 v10, v28, v14
	v_cvt_pk_bf16_f32 v11, v16, v18
	v_cvt_pk_bf16_f32 v12, v20, v22
	v_cvt_pk_bf16_f32 v13, v24, v26
	v_add_co_u32_e32 v14, vcc, s88, v46
	global_store_dwordx4 v[46:47], v[10:13], off
	s_nop 1
	v_cvt_pk_bf16_f32 v10, v29, v15
	v_cvt_pk_bf16_f32 v11, v17, v19
	v_cvt_pk_bf16_f32 v12, v21, v23
	v_cvt_pk_bf16_f32 v13, v25, v27
	v_addc_co_u32_e32 v15, vcc, 0, v47, vcc
	global_store_dwordx4 v[14:15], v[10:13], off
	v_add_co_u32_e32 v14, vcc, s77, v46
	s_waitcnt lgkmcnt(6)
	v_cvt_pk_bf16_f32 v10, v30, v32
	s_waitcnt lgkmcnt(4)
	v_cvt_pk_bf16_f32 v11, v34, v36
	s_waitcnt lgkmcnt(2)
	v_cvt_pk_bf16_f32 v12, v38, v40
	s_waitcnt lgkmcnt(0)
	v_cvt_pk_bf16_f32 v13, v42, v44
	v_addc_co_u32_e32 v15, vcc, 0, v47, vcc
	global_store_dwordx4 v[14:15], v[10:13], off
	v_add_co_u32_e32 v14, vcc, s82, v46
	s_nop 0
	v_cvt_pk_bf16_f32 v10, v31, v33
	v_cvt_pk_bf16_f32 v11, v35, v37
	v_cvt_pk_bf16_f32 v12, v39, v41
	v_cvt_pk_bf16_f32 v13, v43, v45
	v_addc_co_u32_e32 v15, vcc, 0, v47, vcc
	global_store_dwordx4 v[14:15], v[10:13], off
	ds_read2_b32 v[14:15], v51 offset0:97 offset1:105
	ds_read2_b32 v[16:17], v51 offset0:162 offset1:170
	ds_read2_b32 v[18:19], v51 offset0:227 offset1:235
	ds_read2_b32 v[20:21], v56 offset0:36 offset1:44
	ds_read2_b32 v[22:23], v56 offset0:101 offset1:109
	ds_read2_b32 v[24:25], v56 offset0:166 offset1:174
	ds_read2_b32 v[26:27], v56 offset0:231 offset1:239
	ds_read2_b32 v[28:29], v51 offset0:32 offset1:40
	ds_read2_b32 v[30:31], v51 offset0:48 offset1:56
	ds_read2_b32 v[32:33], v51 offset0:113 offset1:121
	ds_read2_b32 v[34:35], v51 offset0:178 offset1:186
	ds_read2_b32 v[36:37], v51 offset0:243 offset1:251
	ds_read2_b32 v[38:39], v56 offset0:52 offset1:60
	ds_read2_b32 v[40:41], v56 offset0:117 offset1:125
	ds_read2_b32 v[42:43], v56 offset0:182 offset1:190
	ds_read2_b32 v[44:45], v56 offset0:247 offset1:255
	v_add_co_u32_e32 v56, vcc, s80, v46
	s_mov_b32 s22, 0x14000
	s_nop 0
	v_addc_co_u32_e32 v57, vcc, 0, v47, vcc
	s_waitcnt lgkmcnt(8)
	v_cvt_pk_bf16_f32 v10, v28, v14
	v_cvt_pk_bf16_f32 v11, v16, v18
	v_cvt_pk_bf16_f32 v12, v20, v22
	v_cvt_pk_bf16_f32 v13, v24, v26
	v_add_co_u32_e32 v14, vcc, s22, v46
	global_store_dwordx4 v[56:57], v[10:13], off
	s_nop 1
	v_cvt_pk_bf16_f32 v10, v29, v15
	v_cvt_pk_bf16_f32 v11, v17, v19
	v_cvt_pk_bf16_f32 v12, v21, v23
	v_cvt_pk_bf16_f32 v13, v25, v27
	v_addc_co_u32_e32 v15, vcc, 0, v47, vcc
	global_store_dwordx4 v[14:15], v[10:13], off
	v_add_co_u32_e32 v14, vcc, s83, v46
	s_waitcnt lgkmcnt(6)
	v_cvt_pk_bf16_f32 v10, v30, v32
	s_waitcnt lgkmcnt(4)
	v_cvt_pk_bf16_f32 v11, v34, v36
	s_waitcnt lgkmcnt(2)
	v_cvt_pk_bf16_f32 v12, v38, v40
	s_waitcnt lgkmcnt(0)
	v_cvt_pk_bf16_f32 v13, v42, v44
	v_addc_co_u32_e32 v15, vcc, 0, v47, vcc
	global_store_dwordx4 v[14:15], v[10:13], off
	v_add_co_u32_e32 v14, vcc, 0x1c000, v46
	s_nop 0
	v_cvt_pk_bf16_f32 v10, v31, v33
	v_cvt_pk_bf16_f32 v11, v35, v37
	v_cvt_pk_bf16_f32 v12, v39, v41
	v_cvt_pk_bf16_f32 v13, v43, v45
	v_addc_co_u32_e32 v15, vcc, 0, v47, vcc
	global_store_dwordx4 v[14:15], v[10:13], off

.LBB0_1416:
	s_andn2_saveexec_b64 s[18:19], s[18:19]
	s_cbranch_execz .LBB0_1418
	v_add_u32_e32 v10, 0xfffff930, v3
	v_lshrrev_b32_e32 v130, 7, v10
	v_lshl_add_u64 v[10:11], s[4:5], 0, v[130:131]
	v_readlane_b32 s36, v251, 35
	v_and_b32_e32 v84, 0x1c0, v52
	v_lshlrev_b64 v[10:11], 21, v[10:11]
	v_readlane_b32 s46, v251, 45
	v_readlane_b32 s47, v251, 46
	v_and_b32_e32 v85, 0x3c0, v55
	v_or_b32_e32 v13, v84, v9
	v_lshl_add_u64 v[10:11], s[46:47], 0, v[10:11]
	v_lshlrev_b64 v[46:47], 20, v[130:131]
	v_or_b32_e32 v12, v85, v48
	v_lshlrev_b32_e32 v130, 12, v13
	v_lshl_add_u64 v[10:11], v[10:11], 0, v[130:131]
	v_lshlrev_b32_e32 v130, 2, v12
	v_lshl_add_u64 v[76:77], v[10:11], 0, v[130:131]
	s_waitcnt lgkmcnt(0)
	v_add_co_u32_e32 v14, vcc, s88, v76
	s_mov_b32 s21, 0x8000
	s_nop 0
	v_addc_co_u32_e32 v15, vcc, 0, v77, vcc
	v_add_co_u32_e32 v18, vcc, s21, v76
	s_mov_b32 s22, 0xc000
	s_nop 0
	v_addc_co_u32_e32 v19, vcc, 0, v77, vcc
	v_add_co_u32_e32 v22, vcc, s22, v76
	s_mov_b32 s20, 0x14000
	s_nop 0
	v_addc_co_u32_e32 v23, vcc, 0, v77, vcc
	v_add_co_u32_e32 v26, vcc, s80, v76
	global_load_dwordx4 v[10:13], v[76:77], off nt
	s_nop 0
	global_load_dwordx4 v[14:17], v[14:15], off nt
	v_addc_co_u32_e32 v27, vcc, 0, v77, vcc
	v_add_co_u32_e32 v30, vcc, s20, v76
	s_mov_b32 s20, 0x1c000
	s_nop 0
	v_addc_co_u32_e32 v31, vcc, 0, v77, vcc
	v_add_co_u32_e32 v34, vcc, s83, v76
	global_load_dwordx4 v[18:21], v[18:19], off nt
	s_nop 0
	global_load_dwordx4 v[22:25], v[22:23], off nt
	v_addc_co_u32_e32 v35, vcc, 0, v77, vcc
	v_add_co_u32_e32 v38, vcc, s20, v76
	s_mov_b32 s20, 0x20000
	s_nop 0
	v_addc_co_u32_e32 v39, vcc, 0, v77, vcc
	v_add_co_u32_e32 v42, vcc, s20, v76
	s_mov_b32 s20, 0x24000
	s_nop 0
	v_addc_co_u32_e32 v43, vcc, 0, v77, vcc
	v_add_co_u32_e32 v56, vcc, s20, v76
	s_mov_b32 s20, 0x28000
	s_nop 0
	v_addc_co_u32_e32 v57, vcc, 0, v77, vcc
	v_add_co_u32_e32 v60, vcc, s20, v76
	s_mov_b32 s20, 0x2c000
	s_nop 0
	v_addc_co_u32_e32 v61, vcc, 0, v77, vcc
	v_add_co_u32_e32 v64, vcc, s20, v76
	s_mov_b32 s20, 0x30000
	s_nop 0
	v_addc_co_u32_e32 v65, vcc, 0, v77, vcc
	v_add_co_u32_e32 v68, vcc, s20, v76
	s_mov_b32 s20, 0x34000
	s_nop 0
	v_addc_co_u32_e32 v69, vcc, 0, v77, vcc
	v_add_co_u32_e32 v72, vcc, s20, v76
	s_mov_b32 s20, 0x38000
	s_nop 0
	v_addc_co_u32_e32 v73, vcc, 0, v77, vcc
	v_add_co_u32_e32 v78, vcc, s20, v76
	s_mov_b32 s20, 0x3c000
	s_nop 0
	v_addc_co_u32_e32 v79, vcc, 0, v77, vcc
	v_add_co_u32_e32 v80, vcc, s20, v76
	global_load_dwordx4 v[26:29], v[26:27], off nt
	s_nop 0
	global_load_dwordx4 v[30:33], v[30:31], off nt
	v_addc_co_u32_e32 v81, vcc, 0, v77, vcc
	global_load_dwordx4 v[34:37], v[34:35], off nt
	s_nop 0
	global_load_dwordx4 v[38:41], v[38:39], off nt
	s_nop 0
	global_load_dwordx4 v[42:45], v[42:43], off nt
	s_nop 0
	global_load_dwordx4 v[56:59], v[56:57], off nt
	s_nop 0
	global_load_dwordx4 v[60:63], v[60:61], off nt
	s_nop 0
	global_load_dwordx4 v[64:67], v[64:65], off nt
	s_nop 0
	global_load_dwordx4 v[68:71], v[68:69], off nt
	s_nop 0
	global_load_dwordx4 v[72:75], v[72:73], off nt
	s_nop 0
	global_load_dwordx4 v[76:79], v[78:79], off nt
	s_nop 0
	global_load_dwordx4 v[80:83], v[80:81], off nt
	v_readlane_b32 s37, v251, 36
	v_readlane_b32 s38, v251, 37
	v_readlane_b32 s39, v251, 38
	v_readlane_b32 s40, v251, 39
	v_readlane_b32 s41, v251, 40
	v_readlane_b32 s42, v251, 41
	v_readlane_b32 s43, v251, 42
	v_readlane_b32 s44, v251, 43
	v_readlane_b32 s45, v251, 44
	v_readlane_b32 s48, v251, 47
	v_readlane_b32 s49, v251, 48
	v_readlane_b32 s50, v251, 49
	v_readlane_b32 s51, v251, 50
	v_lshl_add_u64 v[46:47], s[12:13], 0, v[46:47]
	s_waitcnt vmcnt(0)
	ds_write2_b32 v49, v10, v11 offset1:1
	ds_write2_b32 v49, v12, v13 offset0:2 offset1:3
	v_add_u32_e32 v10, 0x410, v49
	ds_write2_b32 v10, v14, v15 offset1:1
	v_add_u32_e32 v10, 0x418, v49
	ds_write2_b32 v10, v16, v17 offset1:1
	v_add_u32_e32 v10, 0x820, v49
	ds_write2_b32 v10, v18, v19 offset1:1
	v_add_u32_e32 v10, 0x828, v49
	ds_write2_b32 v10, v20, v21 offset1:1
	v_add_u32_e32 v10, 0xc30, v49
	ds_write2_b32 v10, v22, v23 offset1:1
	v_add_u32_e32 v10, 0xc38, v49
	ds_write2_b32 v10, v24, v25 offset1:1
	v_add_u32_e32 v10, 0x1040, v49
	ds_write2_b32 v10, v26, v27 offset1:1
	v_add_u32_e32 v10, 0x1048, v49
	ds_write2_b32 v10, v28, v29 offset1:1
	v_add_u32_e32 v10, 0x1450, v49
	ds_write2_b32 v10, v30, v31 offset1:1
	v_add_u32_e32 v10, 0x1458, v49
	ds_write2_b32 v10, v32, v33 offset1:1
	v_add_u32_e32 v10, 0x1860, v49
	ds_write2_b32 v10, v34, v35 offset1:1
	v_add_u32_e32 v10, 0x1868, v49
	ds_write2_b32 v10, v36, v37 offset1:1
	v_add_u32_e32 v10, 0x1c70, v49
	ds_write2_b32 v10, v38, v39 offset1:1
	v_add_u32_e32 v10, 0x1c78, v49
	ds_write2_b32 v10, v40, v41 offset1:1
	v_add_u32_e32 v10, 0x2080, v49
	ds_write2_b32 v10, v42, v43 offset1:1
	v_add_u32_e32 v10, 0x2088, v49
	ds_write2_b32 v10, v44, v45 offset1:1
	v_add_u32_e32 v10, 0x2490, v49
	ds_write2_b32 v10, v56, v57 offset1:1
	v_add_u32_e32 v10, 0x2498, v49
	ds_write2_b32 v10, v58, v59 offset1:1
	v_add_u32_e32 v10, 0x28a0, v49
	ds_write2_b32 v10, v60, v61 offset1:1
	v_add_u32_e32 v10, 0x28a8, v49
	ds_write2_b32 v10, v62, v63 offset1:1
	v_add_u32_e32 v10, 0x2cb0, v49
	ds_write2_b32 v10, v64, v65 offset1:1
	v_add_u32_e32 v10, 0x2cb8, v49
	ds_write2_b32 v10, v66, v67 offset1:1
	v_add_u32_e32 v10, 0x30c0, v49
	ds_write2_b32 v10, v68, v69 offset1:1
	v_add_u32_e32 v10, 0x30c8, v49
	ds_write2_b32 v10, v70, v71 offset1:1
	v_add_u32_e32 v10, 0x34d0, v49
	ds_write2_b32 v10, v72, v73 offset1:1
	v_add_u32_e32 v10, 0x34d8, v49
	ds_write2_b32 v10, v74, v75 offset1:1
	v_add_u32_e32 v10, 0x38e0, v49
	ds_write2_b32 v10, v76, v77 offset1:1
	v_add_u32_e32 v10, 0x38e8, v49
	ds_write2_b32 v10, v78, v79 offset1:1
	v_add_u32_e32 v10, 0x3cf0, v49
	ds_write2_b32 v10, v80, v81 offset1:1
	v_add_u32_e32 v10, 0x3cf8, v49
	ds_write2_b32 v10, v82, v83 offset1:1
	v_add_u32_e32 v57, 0x400, v51
	ds_read2_b32 v[14:15], v51 offset0:65 offset1:73
	ds_read2_b32 v[16:17], v51 offset0:130 offset1:138
	ds_read2_b32 v[18:19], v51 offset0:195 offset1:203
	ds_read2_b32 v[20:21], v57 offset0:4 offset1:12
	ds_read2_b32 v[22:23], v57 offset0:69 offset1:77
	ds_read2_b32 v[24:25], v57 offset0:134 offset1:142
	ds_read2_b32 v[26:27], v57 offset0:199 offset1:207
	ds_read2_b32 v[28:29], v51 offset1:8
	ds_read2_b32 v[30:31], v51 offset0:16 offset1:24
	ds_read2_b32 v[32:33], v51 offset0:81 offset1:89
	ds_read2_b32 v[34:35], v51 offset0:146 offset1:154
	ds_read2_b32 v[36:37], v51 offset0:211 offset1:219
	ds_read2_b32 v[38:39], v57 offset0:20 offset1:28
	ds_read2_b32 v[40:41], v57 offset0:85 offset1:93
	ds_read2_b32 v[42:43], v57 offset0:150 offset1:158
	ds_read2_b32 v[44:45], v57 offset0:215 offset1:223
	v_lshlrev_b32_e32 v130, 1, v84
	v_lshl_add_u64 v[10:11], v[46:47], 0, v[130:131]
	v_lshlrev_b32_e32 v130, 1, v2
	v_or_b32_e32 v56, v85, v50
	v_lshl_add_u64 v[46:47], v[10:11], 0, v[130:131]
	v_lshlrev_b32_e32 v130, 10, v56
	v_lshl_add_u64 v[46:47], v[46:47], 0, v[130:131]
	s_waitcnt lgkmcnt(8)
	v_cvt_pk_bf16_f32 v10, v28, v14
	v_cvt_pk_bf16_f32 v11, v16, v18
	v_cvt_pk_bf16_f32 v12, v20, v22
	v_cvt_pk_bf16_f32 v13, v24, v26
	v_add_co_u32_e32 v14, vcc, s76, v46
	global_store_dwordx4 v[46:47], v[10:13], off
	s_nop 1
	v_cvt_pk_bf16_f32 v10, v29, v15
	v_cvt_pk_bf16_f32 v11, v17, v19
	v_cvt_pk_bf16_f32 v12, v21, v23
	v_cvt_pk_bf16_f32 v13, v25, v27
	v_addc_co_u32_e32 v15, vcc, 0, v47, vcc
	global_store_dwordx4 v[14:15], v[10:13], off
	v_add_co_u32_e32 v14, vcc, s88, v46
	s_waitcnt lgkmcnt(6)
	v_cvt_pk_bf16_f32 v10, v30, v32
	s_waitcnt lgkmcnt(4)
	v_cvt_pk_bf16_f32 v11, v34, v36
	s_waitcnt lgkmcnt(2)
	v_cvt_pk_bf16_f32 v12, v38, v40
	s_waitcnt lgkmcnt(0)
	v_cvt_pk_bf16_f32 v13, v42, v44
	v_addc_co_u32_e32 v15, vcc, 0, v47, vcc
	global_store_dwordx4 v[14:15], v[10:13], off
	v_add_co_u32_e32 v14, vcc, s75, v46
	s_nop 0
	v_cvt_pk_bf16_f32 v10, v31, v33
	v_cvt_pk_bf16_f32 v11, v35, v37
	v_cvt_pk_bf16_f32 v12, v39, v41
	v_cvt_pk_bf16_f32 v13, v43, v45
	v_addc_co_u32_e32 v15, vcc, 0, v47, vcc
	global_store_dwordx4 v[14:15], v[10:13], off
	ds_read2_b32 v[14:15], v51 offset0:97 offset1:105
	ds_read2_b32 v[16:17], v51 offset0:162 offset1:170
	ds_read2_b32 v[18:19], v51 offset0:227 offset1:235
	ds_read2_b32 v[20:21], v57 offset0:36 offset1:44
	ds_read2_b32 v[22:23], v57 offset0:101 offset1:109
	ds_read2_b32 v[24:25], v57 offset0:166 offset1:174
	ds_read2_b32 v[26:27], v57 offset0:231 offset1:239
	ds_read2_b32 v[28:29], v51 offset0:32 offset1:40
	ds_read2_b32 v[30:31], v51 offset0:48 offset1:56
	ds_read2_b32 v[32:33], v51 offset0:113 offset1:121
	ds_read2_b32 v[34:35], v51 offset0:178 offset1:186
	ds_read2_b32 v[36:37], v51 offset0:243 offset1:251
	ds_read2_b32 v[38:39], v57 offset0:52 offset1:60
	ds_read2_b32 v[40:41], v57 offset0:117 offset1:125
	ds_read2_b32 v[42:43], v57 offset0:182 offset1:190
	ds_read2_b32 v[44:45], v57 offset0:247 offset1:255
	v_add_co_u32_e32 v56, vcc, s21, v46
	s_mov_b32 s20, 0xa000
	s_nop 0
	v_addc_co_u32_e32 v57, vcc, 0, v47, vcc
	s_waitcnt lgkmcnt(8)
	v_cvt_pk_bf16_f32 v10, v28, v14
	v_cvt_pk_bf16_f32 v11, v16, v18
	v_cvt_pk_bf16_f32 v12, v20, v22
	v_cvt_pk_bf16_f32 v13, v24, v26
	v_add_co_u32_e32 v14, vcc, s20, v46
	global_store_dwordx4 v[56:57], v[10:13], off
	s_mov_b32 s77, 0x8000
	s_mov_b32 s82, 0xc000
	v_cvt_pk_bf16_f32 v10, v29, v15
	v_cvt_pk_bf16_f32 v11, v17, v19
	v_cvt_pk_bf16_f32 v12, v21, v23
	v_cvt_pk_bf16_f32 v13, v25, v27
	v_addc_co_u32_e32 v15, vcc, 0, v47, vcc
	global_store_dwordx4 v[14:15], v[10:13], off
	v_add_co_u32_e32 v14, vcc, s22, v46
	s_waitcnt lgkmcnt(6)
	v_cvt_pk_bf16_f32 v10, v30, v32
	s_waitcnt lgkmcnt(4)
	v_cvt_pk_bf16_f32 v11, v34, v36
	s_waitcnt lgkmcnt(2)
	v_cvt_pk_bf16_f32 v12, v38, v40
	s_waitcnt lgkmcnt(0)
	v_cvt_pk_bf16_f32 v13, v42, v44
	v_addc_co_u32_e32 v15, vcc, 0, v47, vcc
	global_store_dwordx4 v[14:15], v[10:13], off
	v_add_co_u32_e32 v14, vcc, 0xe000, v46
	s_nop 0
	v_cvt_pk_bf16_f32 v10, v31, v33
	v_cvt_pk_bf16_f32 v11, v35, v37
	v_cvt_pk_bf16_f32 v12, v39, v41
	v_cvt_pk_bf16_f32 v13, v43, v45
	v_addc_co_u32_e32 v15, vcc, 0, v47, vcc
	global_store_dwordx4 v[14:15], v[10:13], off
